# v036 + row-pass (L1, final) wave reductions use DPP adds for the xor 1/2/4/8 steps
# speedup vs baseline: 1.0091x; 1.0015x over previous
; __device__ __forceinline__ unsigned pk2(float lo, float hi) { unsigned r; asm("v_cvt_pk_bf16_f32 %0, %1, %2" : "=v"(r) : "v"(lo), "v"(hi)); return r; }
; __device__ __forceinline__ float bflo(unsigned w) { return __uint_as_float(w << 16); }
; __device__ __forceinline__ float bfhi(unsigned w) { return __uint_as_float(w & 0xffff0000u); }
; __device__ __forceinline__ float wave_sum(float v) {
;     v += SHX(v, 1); v += SHX(v, 2); v += SHX(v, 4); v += SHX(v, 8); v += SHX(v, 16); v += SHX(v, 32);
;     return v;
; template <int MODE>
; __device__ __forceinline__ void phase_rowpass1(const Ptrs& P, LAS unsigned char* lds, int layer, int tid_, int vcu, int G) {
;     ...
;             f32x4 e[4]; float ss = 0.f;
; #pragma unroll
;             for (int jp = 0; jp < 2; ++jp) { const v4u hw = ((const v4u*)(H + (size_t)row * D))[lane + 64 * jp]; const v4u w = __builtin_nontemporal_load((const v4u*)(GE + (size_t)row * D) + lane + 64 * jp);
;                 v[2 * jp] = (f32x4){bflo(hw.x), bfhi(hw.x), bflo(hw.y), bfhi(hw.y)}; v[2 * jp + 1] = (f32x4){bflo(hw.z), bfhi(hw.z), bflo(hw.w), bfhi(hw.w)};
;                 e[2 * jp] = (f32x4){bflo(w.x), bfhi(w.x), bflo(w.y), bfhi(w.y)}; e[2 * jp + 1] = (f32x4){bflo(w.z), bfhi(w.z), bflo(w.w), bfhi(w.w)}; }
; #pragma unroll
;             for (int j = 0; j < 4; ++j) ss += e[j][0] * e[j][0] + e[j][1] * e[j][1] + e[j][2] * e[j][2] + e[j][3] * e[j][3];
;             const float r = rsqrtf(wave_sum(ss) * (1.f / D) + EPS);
; #pragma unroll
;             for (int j = 0; j < 4; ++j) { const f32x4 g = ((const f32x4*)pg)[F4(j)]; v[j] = v[j] + e[j] * r * g; }
;         }
;         if (MODE != 2) {
; #pragma unroll
;             for (int jp = 0; jp < 2; ++jp) { v4u hw; hw.x = pk2(v[2 * jp][0], v[2 * jp][1]); hw.y = pk2(v[2 * jp][2], v[2 * jp][3]); hw.z = pk2(v[2 * jp + 1][0], v[2 * jp + 1][1]); hw.w = pk2(v[2 * jp + 1][2], v[2 * jp + 1][3]);
;                 ((v4u*)(H + (size_t)row * D))[lane + 64 * jp] = hw; }
;         }
;         float ss = 0.f;
; #pragma unroll
;         for (int j = 0; j < 4; ++j) ss += v[j][0] * v[j][0] + v[j][1] * v[j][1] + v[j][2] * v[j][2] + v[j][3] * v[j][3];
;         const float rstd = rsqrtf(wave_sum(ss) * (1.f / D) + EPS);
; #pragma unroll
;         for (int j = 0; j < 4; ++j) { const f32x4 g = ((const f32x4*)g1)[F4(j)]; v[j] = v[j] * rstd * g; }
.LBB0_266:
	v_lshl_add_u64 v[22:23], s[0:1], 0, v[20:21]
	v_add_co_u32_e32 v24, vcc, 0x34600000, v22
	s_nop 1
	v_addc_co_u32_e32 v25, vcc, 0, v23, vcc
	s_waitcnt vmcnt(2)
	v_lshlrev_b32_e32 v4, 16, v232
	v_and_b32_e32 v5, 0xffff0000, v232
	v_lshlrev_b32_e32 v8, 16, v233
	v_and_b32_e32 v9, 0xffff0000, v233
	s_waitcnt lgkmcnt(0)
	v_lshlrev_b32_e32 v2, 16, v234
	v_and_b32_e32 v3, 0xffff0000, v234
	v_lshlrev_b32_e32 v6, 16, v235
	v_and_b32_e32 v7, 0xffff0000, v235
	v_and_b32_e32 v37, 0xffff0000, v238
	v_and_b32_e32 v36, 0xffff0000, v236
	v_lshlrev_b32_e32 v35, 16, v238
	v_lshlrev_b32_e32 v34, 16, v236
	v_lshlrev_b32_e32 v52, 16, v237
	v_and_b32_e32 v54, 0xffff0000, v237
	v_pk_mul_f32 v[30:31], v[36:37], v[36:37]
	v_lshlrev_b32_e32 v53, 16, v239
	v_and_b32_e32 v55, 0xffff0000, v239
	v_pk_fma_f32 v[30:31], v[34:35], v[34:35], v[30:31]
	v_lshlrev_b32_e32 v46, 16, v240
	v_and_b32_e32 v45, 0xffff0000, v248
	v_and_b32_e32 v44, 0xffff0000, v250
	v_lshlrev_b32_e32 v43, 16, v248
	v_lshlrev_b32_e32 v42, 16, v250
	v_pk_mul_f32 v[32:33], v[44:45], v[44:45]
	v_pk_fma_f32 v[30:31], v[52:53], v[52:53], v[30:31]
	v_lshlrev_b32_e32 v39, 16, v249
	v_lshlrev_b32_e32 v38, 16, v251
	v_pk_fma_f32 v[32:33], v[42:43], v[42:43], v[32:33]
	v_pk_fma_f32 v[30:31], v[54:55], v[54:55], v[30:31]
	v_and_b32_e32 v41, 0xffff0000, v249
	v_and_b32_e32 v40, 0xffff0000, v251
	v_pk_fma_f32 v[32:33], v[38:39], v[38:39], v[32:33]
	v_add_f32_e32 v30, v30, v31
	v_pk_fma_f32 v[32:33], v[40:41], v[40:41], v[32:33]
	v_and_b32_e32 v47, 0xffff0000, v240
	v_add_f32_e32 v30, v30, v33
	v_add_f32_e32 v30, v32, v30
	v_lshlrev_b32_e32 v48, 16, v241
	v_and_b32_e32 v49, 0xffff0000, v241
	v_lshlrev_b32_e32 v26, 16, v242
	v_and_b32_e32 v27, 0xffff0000, v242
	s_waitcnt lgkmcnt(0)
	s_nop 1
	v_add_f32_dpp v30, v30, v30 quad_perm:[1,0,3,2] row_mask:0xf bank_mask:0xf
	v_lshlrev_b32_e32 v28, 16, v243
	v_and_b32_e32 v29, 0xffff0000, v243
	v_add_u32_e32 v160, s74, v10
	v_cmp_gt_i32_e32 vcc, 0x4000, v160
	v_lshl_add_u64 v[160:161], v[20:21], 0, s[94:95]
	s_nop 0
	v_cndmask_b32_e32 v160, v20, v160, vcc
	v_cndmask_b32_e32 v161, v21, v161, vcc
	v_lshl_add_u64 v[160:161], s[0:1], 0, v[160:161]
	v_add_co_u32_e32 v244, vcc, 0x34600000, v160
	s_nop 1
	v_addc_co_u32_e32 v245, vcc, 0, v161, vcc
	v_add_co_u32_e32 v160, vcc, 0x65a00000, v160
	s_nop 1
	v_addc_co_u32_e32 v161, vcc, 0, v161, vcc
	global_load_dwordx4 v[232:235], v[244:245], off
	global_load_dwordx4 v[236:239], v[160:161], off nt
	global_load_dwordx4 v[240:243], v[244:245], off offset:1024
	global_load_dwordx4 v[248:251], v[160:161], off offset:1024 nt
	s_waitcnt lgkmcnt(0)
	s_nop 1
	v_add_f32_dpp v30, v30, v30 quad_perm:[2,3,0,1] row_mask:0xf bank_mask:0xf
	s_waitcnt lgkmcnt(0)
	s_nop 1
	v_add_f32_dpp v30, v30, v30 row_half_mirror row_mask:0xf bank_mask:0xf
	s_waitcnt lgkmcnt(0)
	s_nop 1
	v_add_f32_dpp v30, v30, v30 row_mirror row_mask:0xf bank_mask:0xf
	ds_swizzle_b32 v31, v30 offset:swizzle(SWAP,16)
	s_waitcnt lgkmcnt(0)
	v_add_f32_e32 v30, v30, v31
	v_mbcnt_lo_u32_b32 v31, -1, 0
	s_nop 0
	v_mbcnt_hi_u32_b32 v31, -1, v31
	v_lshlrev_b32_e32 v31, 2, v31
	v_xor_b32_e32 v31, 0x80, v31
	ds_bpermute_b32 v31, v31, v30
	s_waitcnt lgkmcnt(0)
	v_add_f32_e32 v30, v30, v31
	v_fmamk_f32 v30, v30, 0x3a800000, v196
	v_cmp_gt_f32_e32 vcc, s73, v30
	v_mul_f32_e32 v31, 0x4b800000, v30
	s_nop 0
	v_cndmask_b32_e32 v30, v30, v31, vcc
	v_rsq_f32_e32 v30, v30
	s_nop 0
	v_mul_f32_e32 v31, 0x45800000, v30
	v_cndmask_b32_e32 v50, v30, v31, vcc
	v_mov_b32_e32 v30, v34
	v_mov_b32_e32 v31, v36
	v_pk_mul_f32 v[32:33], v[30:31], v[50:51] op_sel_hi:[1,0]
	v_mov_b32_e32 v30, v52
	v_mov_b32_e32 v31, v54
	v_pk_mul_f32 v[30:31], v[30:31], v[50:51] op_sel_hi:[1,0]
	v_mov_b32_e32 v36, v35
	v_mov_b32_e32 v54, v53
	v_mov_b32_e32 v52, v43
	v_mov_b32_e32 v43, v44
	v_mov_b32_e32 v53, v45
	v_pk_mul_f32 v[42:43], v[42:43], v[50:51] op_sel_hi:[1,0]
	v_pk_mul_f32 v[52:53], v[52:53], v[50:51] op_sel_hi:[1,0]
	v_pk_fma_f32 v[30:31], v[66:67], v[30:31], v[8:9]
	v_pk_fma_f32 v[32:33], v[64:65], v[32:33], v[4:5]
	v_pk_mul_f32 v[4:5], v[36:37], v[50:51] op_sel_hi:[1,0]
	v_pk_mul_f32 v[8:9], v[54:55], v[50:51] op_sel_hi:[1,0]
	v_pk_fma_f32 v[36:37], v[68:69], v[4:5], v[2:3]
	v_pk_fma_f32 v[34:35], v[70:71], v[8:9], v[6:7]
	v_mov_b32_e32 v54, v39
	v_mov_b32_e32 v55, v41
	v_mov_b32_e32 v39, v40
	v_pk_mul_f32 v[54:55], v[54:55], v[50:51] op_sel_hi:[1,0]
	v_pk_mul_f32 v[38:39], v[38:39], v[50:51] op_sel_hi:[1,0]
	v_pk_fma_f32 v[2:3], v[76:77], v[42:43], v[26:27]
	v_cvt_pk_bf16_f32 v26, v32, v33
	v_cvt_pk_bf16_f32 v27, v30, v31
	v_pk_fma_f32 v[8:9], v[74:75], v[54:55], v[48:49]
	v_pk_fma_f32 v[6:7], v[72:73], v[52:53], v[46:47]
	v_pk_fma_f32 v[4:5], v[78:79], v[38:39], v[28:29]
	v_cvt_pk_bf16_f32 v28, v36, v37
	v_cvt_pk_bf16_f32 v29, v34, v35
	global_store_dwordx4 v[24:25], v[26:29], off
	s_nop 1
	v_cvt_pk_bf16_f32 v26, v6, v7
	v_cvt_pk_bf16_f32 v27, v8, v9
	v_cvt_pk_bf16_f32 v28, v2, v3
	v_cvt_pk_bf16_f32 v29, v4, v5
	global_store_dwordx4 v[24:25], v[26:29], off offset:1024
	v_mov_b32_e32 v24, v32
	v_mov_b32_e32 v25, v36
	v_mov_b32_e32 v26, v33
	v_mov_b32_e32 v27, v37
	v_pk_mul_f32 v[26:27], v[26:27], v[26:27]
	v_mov_b32_e32 v28, v3
	v_pk_fma_f32 v[24:25], v[24:25], v[24:25], v[26:27]
	v_mov_b32_e32 v26, v30
	v_mov_b32_e32 v27, v34
	v_pk_fma_f32 v[24:25], v[26:27], v[26:27], v[24:25]
	v_mov_b32_e32 v26, v31
	v_mov_b32_e32 v27, v35
	v_mov_b32_e32 v29, v7
	v_pk_fma_f32 v[24:25], v[26:27], v[26:27], v[24:25]
	v_mov_b32_e32 v26, v2
	v_mov_b32_e32 v27, v6
	v_pk_mul_f32 v[28:29], v[28:29], v[28:29]
	v_add_f32_e32 v24, v24, v25
	v_pk_fma_f32 v[26:27], v[26:27], v[26:27], v[28:29]
	v_mov_b32_e32 v28, v4
	v_mov_b32_e32 v29, v8
	v_pk_fma_f32 v[26:27], v[28:29], v[28:29], v[26:27]
	v_mov_b32_e32 v28, v5
	v_mov_b32_e32 v29, v9
	v_pk_fma_f32 v[26:27], v[28:29], v[28:29], v[26:27]
	s_nop 0
	v_add_f32_e32 v24, v27, v24
	v_add_f32_e32 v24, v26, v24
	s_waitcnt lgkmcnt(0)
; #define LAS __attribute__((address_space(3)))
; __device__ __forceinline__ unsigned pk2(float lo, float hi) { unsigned r; asm("v_cvt_pk_bf16_f32 %0, %1, %2" : "=v"(r) : "v"(lo), "v"(hi)); return r; }
; __device__ __forceinline__ float dot2bf(unsigned a, unsigned b, float acc) { return __builtin_amdgcn_fdot2_f32_bf16(__builtin_bit_cast(bf16x2_t, a), __builtin_bit_cast(bf16x2_t, b), acc, false); }
; template <int MODE>
; __device__ __forceinline__ void phase_rowpass1(const Ptrs& P, LAS unsigned char* lds, int layer, int tid_, int vcu, int G) {
;     ...
;         const float rstd = rsqrtf(wave_sum(ss) * (1.f / D) + EPS);
; #pragma unroll
;         for (int j = 0; j < 4; ++j) { const f32x4 g = ((const f32x4*)g1)[F4(j)]; v[j] = v[j] * rstd * g; }
;         if (MODE == 2) {
; #pragma unroll
;             for (int j = 0; j < 4; ++j) ((f32x4*)(P.out + (size_t)row * D))[F4(j)] = v[j];
;         } else {
;             bf16* A = (bf16*)(P.ws + WS_XM) + (size_t)row * D;
;             v4u aw[2];
; #pragma unroll
;             for (int jp = 0; jp < 2; ++jp) { v4u w; w.x = pk2(v[2 * jp][0], v[2 * jp][1]); w.y = pk2(v[2 * jp][2], v[2 * jp][3]); w.z = pk2(v[2 * jp + 1][0], v[2 * jp + 1][1]); w.w = pk2(v[2 * jp + 1][2], v[2 * jp + 1][3]);
;                 ((v4u*)A)[lane + 64 * jp] = w; aw[jp] = w; }
;             float pg[16];
; #pragma unroll
;             for (int g = 0; g < 16; ++g) { float s = 0.f;
; #pragma unroll
;                 for (int jp = 0; jp < 2; ++jp) { const v4u w = *(const LAS v4u*)(gwt + g * 1024 + 8 * lane + 512 * jp); s = dot2bf(aw[jp].x, w.x, s); s = dot2bf(aw[jp].y, w.y, s); s = dot2bf(aw[jp].z, w.z, s); s = dot2bf(aw[jp].w, w.w, s); }
	s_nop 1
	v_add_f32_dpp v24, v24, v24 quad_perm:[1,0,3,2] row_mask:0xf bank_mask:0xf
	s_waitcnt lgkmcnt(0)
	s_nop 1
	v_add_f32_dpp v24, v24, v24 quad_perm:[2,3,0,1] row_mask:0xf bank_mask:0xf
	s_waitcnt lgkmcnt(0)
	s_nop 1
	v_add_f32_dpp v24, v24, v24 row_half_mirror row_mask:0xf bank_mask:0xf
	s_waitcnt lgkmcnt(0)
	s_nop 1
	v_add_f32_dpp v24, v24, v24 row_mirror row_mask:0xf bank_mask:0xf
	ds_swizzle_b32 v25, v24 offset:swizzle(SWAP,16)
	s_waitcnt lgkmcnt(0)
	v_add_f32_e32 v24, v24, v25
	v_mbcnt_lo_u32_b32 v25, -1, 0
	s_nop 0
	v_mbcnt_hi_u32_b32 v25, -1, v25
	s_nop 0
	v_lshlrev_b32_e32 v25, 2, v25
	v_xor_b32_e32 v25, 0x80, v25
	ds_bpermute_b32 v25, v25, v24
	s_waitcnt lgkmcnt(0)
	v_add_f32_e32 v24, v24, v25
	v_fmamk_f32 v24, v24, 0x3a800000, v196
	v_cmp_gt_f32_e32 vcc, s73, v24
	v_mul_f32_e32 v25, 0x4b800000, v24
	s_nop 0
	v_cndmask_b32_e32 v24, v24, v25, vcc
	v_rsq_f32_e32 v24, v24
	s_nop 0
	v_mul_f32_e32 v25, 0x45800000, v24
	v_cndmask_b32_e32 v42, v24, v25, vcc
	v_pk_mul_f32 v[28:29], v[32:33], v[42:43] op_sel_hi:[1,0]
	v_pk_mul_f32 v[30:31], v[30:31], v[42:43] op_sel_hi:[1,0]
	v_pk_mul_f32 v[2:3], v[2:3], v[42:43] op_sel_hi:[1,0]
	v_pk_mul_f32 v[4:5], v[4:5], v[42:43] op_sel_hi:[1,0]
	v_add_co_u32_e32 v22, vcc, s25, v22
	v_pk_mul_f32 v[6:7], v[6:7], v[42:43] op_sel_hi:[1,0]
	v_pk_mul_f32 v[8:9], v[8:9], v[42:43] op_sel_hi:[1,0]
	v_addc_co_u32_e32 v23, vcc, 0, v23, vcc
	v_pk_mul_f32 v[32:33], v[82:83], v[30:31]
	v_pk_mul_f32 v[38:39], v[80:81], v[28:29]
	v_pk_mul_f32 v[28:29], v[36:37], v[42:43] op_sel_hi:[1,0]
	v_pk_mul_f32 v[30:31], v[34:35], v[42:43] op_sel_hi:[1,0]
	v_pk_mul_f32 v[36:37], v[84:85], v[28:29]
	v_pk_mul_f32 v[34:35], v[86:87], v[30:31]
	v_mov_b32_e32 v40, v163
	v_mov_b32_e32 v41, v163
	v_pk_mul_f32 v[26:27], v[94:95], v[4:5]
	v_pk_mul_f32 v[4:5], v[92:93], v[2:3]
	v_pk_mul_f32 v[30:31], v[90:91], v[8:9]
	v_cvt_pk_bf16_f32 v4, v4, v5
	v_cvt_pk_bf16_f32 v5, v26, v27
	v_pk_mul_f32 v[28:29], v[88:89], v[6:7]
	v_cvt_pk_bf16_f32 v6, v38, v39
	v_cvt_pk_bf16_f32 v7, v32, v33
	v_cvt_pk_bf16_f32 v8, v36, v37
	v_cvt_pk_bf16_f32 v9, v34, v35
	global_store_dwordx4 v[22:23], v[6:9], off
	v_cvt_pk_bf16_f32 v2, v28, v29
	v_cvt_pk_bf16_f32 v3, v30, v31
	global_store_dwordx4 v[22:23], v[2:5], off offset:1024
	v_mov_b32_e32 v22, v163
	v_dot2c_f32_bf16_e32 v22, v6, v96
	v_dot2c_f32_bf16_e32 v22, v7, v97
	v_dot2c_f32_bf16_e32 v22, v8, v98
	v_dot2c_f32_bf16_e32 v22, v9, v99
	v_mov_b32_e32 v23, v163
	v_mov_b32_e32 v36, v163
	v_mov_b32_e32 v37, v163
	v_mov_b32_e32 v38, v163
	v_dot2c_f32_bf16_e32 v22, v2, v100
	v_dot2c_f32_bf16_e32 v22, v3, v101
	v_dot2c_f32_bf16_e32 v22, v4, v102
	v_dot2c_f32_bf16_e32 v22, v5, v103
	v_mov_b32_e32 v39, v163
	v_dot2c_f32_bf16_e32 v23, v6, v104
	v_dot2c_f32_bf16_e32 v23, v7, v105
	v_dot2c_f32_bf16_e32 v23, v8, v106
	v_dot2c_f32_bf16_e32 v23, v9, v107
	v_dot2c_f32_bf16_e32 v23, v2, v108
	v_dot2c_f32_bf16_e32 v23, v3, v109
	v_dot2c_f32_bf16_e32 v23, v4, v110
	v_dot2c_f32_bf16_e32 v23, v5, v111
	v_mov_b32_e32 v24, v163
	v_mov_b32_e32 v25, v163
	v_dot2c_f32_bf16_e32 v24, v6, v112
	v_dot2c_f32_bf16_e32 v24, v7, v113
	v_dot2c_f32_bf16_e32 v24, v8, v114
	v_dot2c_f32_bf16_e32 v24, v9, v115
	v_dot2c_f32_bf16_e32 v24, v2, v116
	v_dot2c_f32_bf16_e32 v24, v3, v117
	v_dot2c_f32_bf16_e32 v24, v4, v118
	v_dot2c_f32_bf16_e32 v24, v5, v119
	v_dot2c_f32_bf16_e32 v25, v6, v120
	v_dot2c_f32_bf16_e32 v25, v7, v121
	v_dot2c_f32_bf16_e32 v25, v8, v122
	v_dot2c_f32_bf16_e32 v25, v9, v123
	v_dot2c_f32_bf16_e32 v25, v2, v124
	v_dot2c_f32_bf16_e32 v25, v3, v125
	v_dot2c_f32_bf16_e32 v25, v4, v126
	v_dot2c_f32_bf16_e32 v25, v5, v127
	v_mov_b32_e32 v26, v163
	v_mov_b32_e32 v27, v163
	v_dot2c_f32_bf16_e32 v26, v6, v128
	v_dot2c_f32_bf16_e32 v26, v7, v129
	v_dot2c_f32_bf16_e32 v26, v8, v130
	v_dot2c_f32_bf16_e32 v26, v9, v131
	v_dot2c_f32_bf16_e32 v26, v2, v132
	v_dot2c_f32_bf16_e32 v26, v3, v133
	v_dot2c_f32_bf16_e32 v26, v4, v134
	v_dot2c_f32_bf16_e32 v26, v5, v135
	v_dot2c_f32_bf16_e32 v27, v6, v136
	v_dot2c_f32_bf16_e32 v27, v7, v137
	v_dot2c_f32_bf16_e32 v27, v8, v138
	v_dot2c_f32_bf16_e32 v27, v9, v139
	v_dot2c_f32_bf16_e32 v27, v2, v140
	v_dot2c_f32_bf16_e32 v27, v3, v141
	v_dot2c_f32_bf16_e32 v27, v4, v142
	v_dot2c_f32_bf16_e32 v27, v5, v143
	v_mov_b32_e32 v28, v163
	v_mov_b32_e32 v29, v163
	v_dot2c_f32_bf16_e32 v28, v6, v144
	v_dot2c_f32_bf16_e32 v28, v7, v145
	v_dot2c_f32_bf16_e32 v28, v8, v146
	v_dot2c_f32_bf16_e32 v28, v9, v147
	v_dot2c_f32_bf16_e32 v28, v2, v148
	v_dot2c_f32_bf16_e32 v28, v3, v149
	v_dot2c_f32_bf16_e32 v28, v4, v150
	v_dot2c_f32_bf16_e32 v28, v5, v151
	v_dot2c_f32_bf16_e32 v29, v6, v152
	v_dot2c_f32_bf16_e32 v29, v7, v153
	v_dot2c_f32_bf16_e32 v29, v8, v154
	v_dot2c_f32_bf16_e32 v29, v9, v155
	v_dot2c_f32_bf16_e32 v29, v2, v156
	v_dot2c_f32_bf16_e32 v29, v3, v157
	v_dot2c_f32_bf16_e32 v29, v4, v158
	v_dot2c_f32_bf16_e32 v29, v5, v159
	v_mov_b32_e32 v30, v163
	v_mov_b32_e32 v31, v163
	v_dot2c_f32_bf16_e32 v30, v6, v168
	v_dot2c_f32_bf16_e32 v30, v7, v169
	v_dot2c_f32_bf16_e32 v30, v8, v170
	v_dot2c_f32_bf16_e32 v30, v9, v171
	v_dot2c_f32_bf16_e32 v30, v2, v172
	v_dot2c_f32_bf16_e32 v30, v3, v173
	v_dot2c_f32_bf16_e32 v30, v4, v174
	v_dot2c_f32_bf16_e32 v30, v5, v175
	v_dot2c_f32_bf16_e32 v31, v6, v176
	v_dot2c_f32_bf16_e32 v31, v7, v177
	v_dot2c_f32_bf16_e32 v31, v8, v178
	v_dot2c_f32_bf16_e32 v31, v9, v179
	v_dot2c_f32_bf16_e32 v31, v2, v180
	v_dot2c_f32_bf16_e32 v31, v3, v181
	v_dot2c_f32_bf16_e32 v31, v4, v182
	v_dot2c_f32_bf16_e32 v31, v5, v183
	v_dot2c_f32_bf16_e32 v36, v6, v184
	v_dot2c_f32_bf16_e32 v36, v7, v185
	v_dot2c_f32_bf16_e32 v36, v8, v186
	v_dot2c_f32_bf16_e32 v36, v9, v187
; #define LAS __attribute__((address_space(3)))
; __device__ __forceinline__ float logsigf_(float x) { return fminf(x, 0.f) - __logf(1.f + __expf(-fabsf(x))); }
; #define SHX(v, m) (((m) < 32) ? __int_as_float(__builtin_amdgcn_ds_swizzle(__float_as_int(v), ((((m) & 31) << 10) | 0x1f))) : shx32(v))
; __device__ __forceinline__ float dot2bf(unsigned a, unsigned b, float acc) { return __builtin_amdgcn_fdot2_f32_bf16(__builtin_bit_cast(bf16x2_t, a), __builtin_bit_cast(bf16x2_t, b), acc, false); }
; template <int MODE>
; __device__ __forceinline__ void phase_rowpass1(const Ptrs& P, LAS unsigned char* lds, int layer, int tid_, int vcu, int G) {
;     ...
;             for (int g = 0; g < 16; ++g) { float s = 0.f;
; #pragma unroll
;                 for (int jp = 0; jp < 2; ++jp) { const v4u w = *(const LAS v4u*)(gwt + g * 1024 + 8 * lane + 512 * jp); s = dot2bf(aw[jp].x, w.x, s); s = dot2bf(aw[jp].y, w.y, s); s = dot2bf(aw[jp].z, w.z, s); s = dot2bf(aw[jp].w, w.w, s); }
;                 pg[g] = s; }
;             float p8[8], p4[4], p2[2], p1;
;             { const bool hi = (lane & 32) != 0;
; #pragma unroll
;               for (int i = 0; i < 8; ++i) { const float send = hi ? pg[i] : pg[8 + i], keep = hi ? pg[8 + i] : pg[i]; p8[i] = keep + SHX(send, 32); } }
;             { const bool hi = (lane & 16) != 0;
; #pragma unroll
;               for (int i = 0; i < 4; ++i) { const float send = hi ? p8[i] : p8[4 + i], keep = hi ? p8[4 + i] : p8[i]; p4[i] = keep + SHX(send, 16); } }
;             { const bool hi = (lane & 8) != 0;
; #pragma unroll
;               for (int i = 0; i < 2; ++i) { const float send = hi ? p4[i] : p4[2 + i], keep = hi ? p4[2 + i] : p4[i]; p2[i] = keep + SHX(send, 8); } }
;             { const bool hi = (lane & 4) != 0; const float send = hi ? p2[0] : p2[1], keep = hi ? p2[1] : p2[0]; p1 = keep + SHX(send, 4); }
;             p1 += SHX(p1, 2); p1 += SHX(p1, 1);
;             const int src = (((lane >> 3) & 1) << 5) | (((lane >> 2) & 1) << 4) | (((lane >> 1) & 1) << 3) | ((lane & 1) << 2);
;             const float mine = __int_as_float(__builtin_amdgcn_ds_bpermute(src << 2, __float_as_int(p1)));
;             if (lane < 16) { float gv = mine + P.gate_b[layer * 16 + lane]; if ((lane >> 2) & 1) gv = logsigf_(gv); ((float*)(P.ws + WS_GATES))[(size_t)row * 16 + lane] = gv; }
	v_dot2c_f32_bf16_e32 v36, v2, v188
	v_dot2c_f32_bf16_e32 v36, v3, v189
	v_dot2c_f32_bf16_e32 v36, v4, v190
	v_dot2c_f32_bf16_e32 v36, v5, v191
	v_dot2c_f32_bf16_e32 v37, v6, v192
	v_dot2c_f32_bf16_e32 v37, v7, v193
	v_dot2c_f32_bf16_e32 v37, v8, v194
	v_dot2c_f32_bf16_e32 v37, v9, v195
	v_dot2c_f32_bf16_e32 v37, v2, v200
	v_dot2c_f32_bf16_e32 v37, v3, v201
	v_dot2c_f32_bf16_e32 v37, v4, v202
	v_dot2c_f32_bf16_e32 v37, v5, v203
	v_dot2c_f32_bf16_e32 v38, v6, v204
	v_dot2c_f32_bf16_e32 v38, v7, v205
	v_dot2c_f32_bf16_e32 v38, v8, v206
	v_dot2c_f32_bf16_e32 v38, v9, v207
	v_dot2c_f32_bf16_e32 v38, v2, v208
	v_dot2c_f32_bf16_e32 v38, v3, v209
	v_dot2c_f32_bf16_e32 v38, v4, v210
	v_dot2c_f32_bf16_e32 v38, v5, v211
	v_dot2c_f32_bf16_e32 v39, v6, v212
	v_dot2c_f32_bf16_e32 v39, v7, v213
	v_dot2c_f32_bf16_e32 v39, v8, v214
	v_dot2c_f32_bf16_e32 v39, v9, v215
	v_dot2c_f32_bf16_e32 v39, v2, v216
	v_dot2c_f32_bf16_e32 v39, v3, v217
	v_dot2c_f32_bf16_e32 v39, v4, v218
	v_dot2c_f32_bf16_e32 v39, v5, v219
	v_dot2c_f32_bf16_e32 v40, v6, v220
	v_dot2c_f32_bf16_e32 v40, v7, v221
	v_dot2c_f32_bf16_e32 v40, v8, v222
	v_dot2c_f32_bf16_e32 v40, v9, v223
	v_dot2c_f32_bf16_e32 v40, v2, v224
	v_dot2c_f32_bf16_e32 v40, v3, v225
	v_dot2c_f32_bf16_e32 v40, v4, v226
	v_dot2c_f32_bf16_e32 v40, v5, v227
	v_dot2c_f32_bf16_e32 v41, v6, v228
	v_dot2c_f32_bf16_e32 v41, v7, v229
	v_dot2c_f32_bf16_e32 v41, v8, v230
	v_dot2c_f32_bf16_e32 v41, v9, v231
	ds_read_b128 v[6:9], v11 offset:31744
	s_waitcnt lgkmcnt(0)
	v_dot2c_f32_bf16_e32 v41, v2, v6
	v_dot2c_f32_bf16_e32 v41, v3, v7
	v_dot2c_f32_bf16_e32 v41, v4, v8
	v_mbcnt_lo_u32_b32 v4, -1, 0
	v_cndmask_b32_e64 v2, v22, v30, s[38:39]
	v_mbcnt_hi_u32_b32 v4, -1, v4
	v_dot2c_f32_bf16_e32 v41, v5, v9
	v_lshlrev_b32_e32 v4, 2, v4
	v_xor_b32_e32 v4, 0x80, v4
	ds_bpermute_b32 v2, v4, v2
	v_mbcnt_lo_u32_b32 v5, -1, 0
	v_cndmask_b32_e64 v3, v30, v22, s[38:39]
	v_mbcnt_hi_u32_b32 v5, -1, v5
	v_mbcnt_lo_u32_b32 v6, -1, 0
	s_waitcnt lgkmcnt(0)
	v_add_f32_e32 v2, v3, v2
	v_lshlrev_b32_e32 v5, 2, v5
	v_cndmask_b32_e64 v3, v23, v31, s[38:39]
	v_xor_b32_e32 v5, 0x80, v5
	ds_bpermute_b32 v3, v5, v3
	v_mbcnt_hi_u32_b32 v6, -1, v6
	v_cndmask_b32_e64 v4, v31, v23, s[38:39]
	v_lshlrev_b32_e32 v6, 2, v6
	v_xor_b32_e32 v6, 0x80, v6
	s_waitcnt lgkmcnt(0)
	v_add_f32_e32 v3, v4, v3
	v_cndmask_b32_e64 v4, v24, v36, s[38:39]
	ds_bpermute_b32 v4, v6, v4
	v_mbcnt_lo_u32_b32 v7, -1, 0
	v_cndmask_b32_e64 v5, v36, v24, s[38:39]
	v_mbcnt_hi_u32_b32 v7, -1, v7
	v_mbcnt_lo_u32_b32 v8, -1, 0
	s_waitcnt lgkmcnt(0)
	v_add_f32_e32 v4, v5, v4
	v_lshlrev_b32_e32 v7, 2, v7
	v_cndmask_b32_e64 v5, v25, v37, s[38:39]
	v_xor_b32_e32 v7, 0x80, v7
	ds_bpermute_b32 v5, v7, v5
	v_mbcnt_hi_u32_b32 v8, -1, v8
	v_cndmask_b32_e64 v6, v37, v25, s[38:39]
	v_lshlrev_b32_e32 v8, 2, v8
	v_xor_b32_e32 v8, 0x80, v8
	s_waitcnt lgkmcnt(0)
	v_add_f32_e32 v5, v6, v5
	v_cndmask_b32_e64 v6, v26, v38, s[38:39]
	ds_bpermute_b32 v6, v8, v6
	v_mbcnt_lo_u32_b32 v9, -1, 0
	v_cndmask_b32_e64 v7, v38, v26, s[38:39]
	v_mbcnt_hi_u32_b32 v9, -1, v9
	v_mbcnt_lo_u32_b32 v22, -1, 0
	s_waitcnt lgkmcnt(0)
	v_add_f32_e32 v6, v7, v6
	v_lshlrev_b32_e32 v9, 2, v9
	v_cndmask_b32_e64 v7, v27, v39, s[38:39]
	v_xor_b32_e32 v9, 0x80, v9
	ds_bpermute_b32 v7, v9, v7
	v_mbcnt_hi_u32_b32 v22, -1, v22
	v_cndmask_b32_e64 v8, v39, v27, s[38:39]
	v_lshlrev_b32_e32 v22, 2, v22
	v_xor_b32_e32 v22, 0x80, v22
	s_waitcnt lgkmcnt(0)
	v_add_f32_e32 v7, v8, v7
	v_cndmask_b32_e64 v8, v28, v40, s[38:39]
	ds_bpermute_b32 v8, v22, v8
	v_mbcnt_lo_u32_b32 v23, -1, 0
	v_cndmask_b32_e64 v9, v40, v28, s[38:39]
	v_mbcnt_hi_u32_b32 v23, -1, v23
	v_cndmask_b32_e64 v22, v41, v29, s[38:39]
	v_lshlrev_b32_e32 v23, 2, v23
	s_waitcnt lgkmcnt(0)
	v_add_f32_e32 v8, v9, v8
	v_cndmask_b32_e64 v9, v29, v41, s[38:39]
	v_xor_b32_e32 v23, 0x80, v23
	ds_bpermute_b32 v9, v23, v9
	s_waitcnt lgkmcnt(0)
	v_add_f32_e32 v9, v22, v9
	v_cndmask_b32_e64 v22, v2, v6, s[40:41]
	v_cndmask_b32_e64 v2, v6, v2, s[40:41]
	ds_swizzle_b32 v6, v22 offset:swizzle(SWAP,16)
	s_waitcnt lgkmcnt(0)
	v_add_f32_e32 v2, v2, v6
	v_cndmask_b32_e64 v6, v3, v7, s[40:41]
	ds_swizzle_b32 v6, v6 offset:swizzle(SWAP,16)
	v_cndmask_b32_e64 v3, v7, v3, s[40:41]
	s_waitcnt lgkmcnt(0)
	v_add_f32_e32 v3, v3, v6
	v_cndmask_b32_e64 v6, v4, v8, s[40:41]
	ds_swizzle_b32 v6, v6 offset:swizzle(SWAP,16)
	v_cndmask_b32_e64 v4, v8, v4, s[40:41]
	s_waitcnt lgkmcnt(0)
	v_add_f32_e32 v4, v4, v6
	v_cndmask_b32_e64 v6, v5, v9, s[40:41]
	ds_swizzle_b32 v6, v6 offset:swizzle(SWAP,16)
	v_cndmask_b32_e64 v5, v9, v5, s[40:41]
	s_waitcnt lgkmcnt(0)
	v_add_f32_e32 v5, v5, v6
	v_cndmask_b32_e64 v6, v2, v4, s[42:43]
	v_cndmask_b32_e64 v2, v4, v2, s[42:43]
	ds_swizzle_b32 v4, v6 offset:swizzle(SWAP,8)
	s_waitcnt lgkmcnt(0)
	v_add_f32_e32 v2, v2, v4
	v_cndmask_b32_e64 v4, v3, v5, s[42:43]
	ds_swizzle_b32 v4, v4 offset:swizzle(SWAP,8)
	v_cndmask_b32_e64 v3, v5, v3, s[42:43]
	s_waitcnt lgkmcnt(0)
	v_add_f32_e32 v3, v3, v4
	v_cndmask_b32_e64 v4, v2, v3, s[44:45]
	v_cndmask_b32_e64 v2, v3, v2, s[44:45]
	ds_swizzle_b32 v3, v4 offset:swizzle(SWAP,4)
	s_waitcnt lgkmcnt(0)
	v_add_f32_e32 v2, v2, v3
	ds_swizzle_b32 v3, v2 offset:swizzle(SWAP,2)
	s_waitcnt lgkmcnt(0)
	v_add_f32_e32 v2, v2, v3
	s_waitcnt lgkmcnt(0)
	s_nop 1
	v_add_f32_dpp v2, v2, v2 quad_perm:[1,0,3,2] row_mask:0xf bank_mask:0xf
	ds_bpermute_b32 v2, v1, v2
	s_and_saveexec_b64 s[8:9], s[46:47]
	s_cbranch_execz .LBB0_265
	s_waitcnt lgkmcnt(0)
	v_add_f32_e32 v2, v246, v2
	s_and_saveexec_b64 s[18:19], s[48:49]
	s_cbranch_execz .LBB0_264
	s_mov_b32 s4, 0xbfb8aa3b
	v_mul_f32_e64 v3, |v2|, s4
	v_exp_f32_e32 v3, v3
	s_mov_b32 s4, 0x3f317217
	v_max_f32_e32 v2, v2, v2
	v_min_f32_e32 v2, 0, v2
	v_add_f32_e32 v3, 1.0, v3
	v_cmp_gt_f32_e32 vcc, s73, v3
	s_nop 1
	v_cndmask_b32_e64 v4, 0, 32, vcc
	v_ldexp_f32 v3, v3, v4
	v_log_f32_e32 v3, v3
	s_nop 0
	v_mul_f32_e32 v4, 0x3f317217, v3
	v_fma_f32 v4, v3, s4, -v4
	v_fmac_f32_e32 v4, 0x3377d1cf, v3
	s_mov_b32 s4, 0x7f800000
	v_fmac_f32_e32 v4, 0x3f317217, v3
	v_cmp_lt_f32_e64 s[50:51], |v3|, s4
	s_nop 1
	v_cndmask_b32_e64 v3, v3, v4, s[50:51]
	v_cndmask_b32_e32 v4, 0, v247, vcc
	v_sub_f32_e32 v3, v3, v4
	v_sub_f32_e32 v2, v2, v3
	s_branch .LBB0_264

; __device__ __forceinline__ unsigned pk2(float lo, float hi) { unsigned r; asm("v_cvt_pk_bf16_f32 %0, %1, %2" : "=v"(r) : "v"(lo), "v"(hi)); return r; }
; template <int MODE>
; __device__ __forceinline__ void phase_rowpass1(const Ptrs& P, LAS unsigned char* lds, int layer, int tid_, int vcu, int G) {
;     ...
;         if (MODE == 0) {
; #pragma unroll
;             for (int j = 0; j < 4; ++j) v[j] = ((const f32x4*)(P.x + (size_t)row * D))[F4(j)];
;         } else {
;             f32x4 e[4]; float ss = 0.f;
; #pragma unroll
;             for (int jp = 0; jp < 2; ++jp) { const v4u hw = ((const v4u*)(H + (size_t)row * D))[lane + 64 * jp]; const v4u w = __builtin_nontemporal_load((const v4u*)(GE + (size_t)row * D) + lane + 64 * jp);
;                 v[2 * jp] = (f32x4){bflo(hw.x), bfhi(hw.x), bflo(hw.y), bfhi(hw.y)}; v[2 * jp + 1] = (f32x4){bflo(hw.z), bfhi(hw.z), bflo(hw.w), bfhi(hw.w)};
;                 e[2 * jp] = (f32x4){bflo(w.x), bfhi(w.x), bflo(w.y), bfhi(w.y)}; e[2 * jp + 1] = (f32x4){bflo(w.z), bfhi(w.z), bflo(w.w), bfhi(w.w)}; }
; #pragma unroll
;             for (int j = 0; j < 4; ++j) ss += e[j][0] * e[j][0] + e[j][1] * e[j][1] + e[j][2] * e[j][2] + e[j][3] * e[j][3];
;             const float r = rsqrtf(wave_sum(ss) * (1.f / D) + EPS);
; #pragma unroll
;             for (int j = 0; j < 4; ++j) { const f32x4 g = ((const f32x4*)pg)[F4(j)]; v[j] = v[j] + e[j] * r * g; }
;         }
;         if (MODE != 2) {
; #pragma unroll
;             for (int jp = 0; jp < 2; ++jp) { v4u hw; hw.x = pk2(v[2 * jp][0], v[2 * jp][1]); hw.y = pk2(v[2 * jp][2], v[2 * jp][3]); hw.z = pk2(v[2 * jp + 1][0], v[2 * jp + 1][1]); hw.w = pk2(v[2 * jp + 1][2], v[2 * jp + 1][3]);
;                 ((v4u*)(H + (size_t)row * D))[lane + 64 * jp] = hw; }
;         }
;         float ss = 0.f;
; #pragma unroll
;         for (int j = 0; j < 4; ++j) ss += v[j][0] * v[j][0] + v[j][1] * v[j][1] + v[j][2] * v[j][2] + v[j][3] * v[j][3];
;         const float rstd = rsqrtf(wave_sum(ss) * (1.f / D) + EPS);
; #pragma unroll
;         for (int j = 0; j < 4; ++j) { const f32x4 g = ((const f32x4*)g1)[F4(j)]; v[j] = v[j] * rstd * g; }
;         if (MODE == 2) {
; #pragma unroll
;             for (int j = 0; j < 4; ++j) ((f32x4*)(P.out + (size_t)row * D))[F4(j)] = v[j];
;         } else {
;             bf16* A = (bf16*)(P.ws + WS_XM) + (size_t)row * D;
;             v4u aw[2];
; #pragma unroll
.LBB0_279:
	global_load_dwordx4 v[10:13], v[28:29], off offset:-2048
	global_load_dwordx4 v[14:17], v[28:29], off offset:-2064
	s_waitcnt lgkmcnt(0)
	global_load_dwordx4 v[2:5], v[28:29], off
	global_load_dwordx4 v[6:9], v[28:29], off offset:-16
	v_lshl_add_u64 v[30:31], s[0:1], 0, v[26:27]
	s_mov_b32 s4, 0x34600000
	v_add_co_u32_e64 v38, s[48:49], s4, v30
	s_waitcnt vmcnt(3)
	v_cvt_pk_bf16_f32 v36, v10, v11
	v_cvt_pk_bf16_f32 v37, v12, v13
	s_nop 0
	v_addc_co_u32_e64 v39, s[48:49], 0, v31, s[48:49]
	s_waitcnt vmcnt(2)
	v_cvt_pk_bf16_f32 v34, v14, v15
	v_cvt_pk_bf16_f32 v35, v16, v17
	global_store_dwordx4 v[38:39], v[34:37], off
	s_waitcnt vmcnt(2)
	s_nop 0
	v_cvt_pk_bf16_f32 v36, v2, v3
	v_cvt_pk_bf16_f32 v37, v4, v5
	s_waitcnt vmcnt(1)
	v_cvt_pk_bf16_f32 v34, v6, v7
	v_cvt_pk_bf16_f32 v35, v8, v9
	global_store_dwordx4 v[38:39], v[34:37], off offset:1024
	v_mov_b32_e32 v38, v7
	v_mov_b32_e32 v39, v3
	v_mov_b32_e32 v36, v15
	v_mov_b32_e32 v37, v11
	v_mov_b32_e32 v34, v14
	v_mov_b32_e32 v35, v10
	v_pk_mul_f32 v[36:37], v[36:37], v[36:37]
	v_pk_mul_f32 v[38:39], v[38:39], v[38:39]
	v_pk_fma_f32 v[34:35], v[34:35], v[34:35], v[36:37]
	v_mov_b32_e32 v36, v16
	v_mov_b32_e32 v37, v12
	v_pk_fma_f32 v[34:35], v[36:37], v[36:37], v[34:35]
	v_mov_b32_e32 v36, v17
	v_mov_b32_e32 v37, v13
	v_pk_fma_f32 v[34:35], v[36:37], v[36:37], v[34:35]
	v_mov_b32_e32 v36, v6
	v_mov_b32_e32 v37, v2
	v_pk_fma_f32 v[36:37], v[36:37], v[36:37], v[38:39]
	v_mov_b32_e32 v38, v8
	v_mov_b32_e32 v39, v4
	v_pk_fma_f32 v[36:37], v[38:39], v[38:39], v[36:37]
	v_mov_b32_e32 v38, v9
	v_mov_b32_e32 v39, v5
	v_pk_fma_f32 v[36:37], v[38:39], v[38:39], v[36:37]
	v_add_f32_e32 v19, v34, v35
	v_add_f32_e32 v19, v19, v36
	v_add_f32_e32 v19, v19, v37
	s_waitcnt lgkmcnt(0)
	s_nop 1
	v_add_f32_dpp v19, v19, v19 quad_perm:[1,0,3,2] row_mask:0xf bank_mask:0xf
	s_waitcnt lgkmcnt(0)
	s_nop 1
	v_add_f32_dpp v19, v19, v19 quad_perm:[2,3,0,1] row_mask:0xf bank_mask:0xf
	s_waitcnt lgkmcnt(0)
	s_nop 1
	v_add_f32_dpp v19, v19, v19 row_half_mirror row_mask:0xf bank_mask:0xf
	s_waitcnt lgkmcnt(0)
	s_nop 1
	v_add_f32_dpp v19, v19, v19 row_mirror row_mask:0xf bank_mask:0xf
	ds_swizzle_b32 v33, v19 offset:swizzle(SWAP,16)
	s_waitcnt lgkmcnt(0)
	v_add_f32_e32 v19, v19, v33
	v_mbcnt_lo_u32_b32 v33, -1, 0
	s_nop 0
	v_mbcnt_hi_u32_b32 v33, -1, v33
	global_load_dwordx4 v[34:37], v[20:21], off offset:16
	global_load_dwordx4 v[38:41], v[20:21], off
	v_lshlrev_b32_e32 v33, 2, v33
	v_xor_b32_e32 v33, 0x80, v33
	ds_bpermute_b32 v33, v33, v19
	s_waitcnt lgkmcnt(0)
	v_add_f32_e32 v19, v19, v33
	v_fmamk_f32 v19, v19, 0x3a800000, v196
	v_cmp_gt_f32_e64 s[48:49], s73, v19
	v_mul_f32_e32 v33, 0x4b800000, v19
	s_nop 0
	v_cndmask_b32_e64 v19, v19, v33, s[48:49]
	v_rsq_f32_e32 v19, v19
	s_nop 0
	v_mul_f32_e32 v33, 0x45800000, v19
	v_cndmask_b32_e64 v42, v19, v33, s[48:49]
	v_pk_mul_f32 v[14:15], v[14:15], v[42:43] op_sel_hi:[1,0]
	v_pk_mul_f32 v[16:17], v[16:17], v[42:43] op_sel_hi:[1,0]
	v_pk_mul_f32 v[10:11], v[10:11], v[42:43] op_sel_hi:[1,0]
	v_pk_mul_f32 v[12:13], v[12:13], v[42:43] op_sel_hi:[1,0]
	v_pk_mul_f32 v[2:3], v[2:3], v[42:43] op_sel_hi:[1,0]
	v_pk_mul_f32 v[4:5], v[4:5], v[42:43] op_sel_hi:[1,0]
	v_pk_mul_f32 v[6:7], v[6:7], v[42:43] op_sel_hi:[1,0]
	v_pk_mul_f32 v[8:9], v[8:9], v[42:43] op_sel_hi:[1,0]
	v_mov_b32_e32 v19, v163
	v_mov_b32_e32 v33, v163
	v_mov_b32_e32 v42, v163
	s_waitcnt vmcnt(1)
	v_pk_mul_f32 v[36:37], v[36:37], v[12:13]
	s_waitcnt vmcnt(0)
	v_pk_mul_f32 v[40:41], v[40:41], v[16:17]
	v_pk_mul_f32 v[38:39], v[38:39], v[14:15]
	v_pk_mul_f32 v[34:35], v[34:35], v[10:11]
	global_load_dwordx4 v[10:13], v[20:21], off offset:2064
	global_load_dwordx4 v[14:17], v[20:21], off offset:2048
	s_waitcnt vmcnt(1)
	v_pk_mul_f32 v[12:13], v[12:13], v[4:5]
	v_pk_mul_f32 v[4:5], v[10:11], v[2:3]
	v_add_co_u32_e64 v10, s[48:49], s25, v30
	s_waitcnt vmcnt(0)
	v_pk_mul_f32 v[16:17], v[16:17], v[8:9]
	v_addc_co_u32_e64 v11, s[48:49], 0, v31, s[48:49]
	v_pk_mul_f32 v[14:15], v[14:15], v[6:7]
	v_cvt_pk_bf16_f32 v6, v38, v39
	v_cvt_pk_bf16_f32 v7, v40, v41
	v_cvt_pk_bf16_f32 v8, v34, v35
	v_cvt_pk_bf16_f32 v9, v36, v37
	global_store_dwordx4 v[10:11], v[6:9], off
	v_cvt_pk_bf16_f32 v2, v14, v15
	v_cvt_pk_bf16_f32 v3, v16, v17
	v_cvt_pk_bf16_f32 v4, v4, v5
	v_cvt_pk_bf16_f32 v5, v12, v13
	global_store_dwordx4 v[10:11], v[2:5], off offset:1024
	v_add_u32_e32 v11, 0, v1
	ds_read_b128 v[12:15], v11
	ds_read_b128 v[34:37], v11 offset:6144
	v_mov_b32_e32 v10, v163
	v_mov_b32_e32 v30, v163
	v_mov_b32_e32 v31, v163
	s_waitcnt lgkmcnt(1)
	v_dot2c_f32_bf16_e32 v10, v6, v12
	v_dot2c_f32_bf16_e32 v10, v7, v13
	v_dot2c_f32_bf16_e32 v10, v8, v14
	v_dot2c_f32_bf16_e32 v10, v9, v15
	ds_read_b128 v[12:15], v11 offset:1024
	v_mov_b32_e32 v38, v163
	v_mov_b32_e32 v39, v163
	v_mov_b32_e32 v40, v163
	v_mov_b32_e32 v41, v163
	s_waitcnt lgkmcnt(0)
	v_dot2c_f32_bf16_e32 v10, v2, v12
	v_dot2c_f32_bf16_e32 v10, v3, v13
	v_dot2c_f32_bf16_e32 v10, v4, v14
	v_dot2c_f32_bf16_e32 v10, v5, v15
	ds_read_b128 v[14:17], v11 offset:2048
	v_mov_b32_e32 v12, v163
	v_mov_b32_e32 v13, v163
	s_waitcnt lgkmcnt(0)
	v_dot2c_f32_bf16_e32 v12, v6, v14
	v_dot2c_f32_bf16_e32 v12, v7, v15
	v_dot2c_f32_bf16_e32 v12, v8, v16
	v_dot2c_f32_bf16_e32 v12, v9, v17
	ds_read_b128 v[14:17], v11 offset:3072
	s_waitcnt lgkmcnt(0)
	v_dot2c_f32_bf16_e32 v12, v2, v14
	v_dot2c_f32_bf16_e32 v12, v3, v15
	v_dot2c_f32_bf16_e32 v12, v4, v16
	v_dot2c_f32_bf16_e32 v12, v5, v17
	ds_read_b128 v[14:17], v11 offset:4096
	s_waitcnt lgkmcnt(0)
	v_dot2c_f32_bf16_e32 v13, v6, v14
	v_dot2c_f32_bf16_e32 v13, v7, v15
	v_dot2c_f32_bf16_e32 v13, v8, v16
	v_dot2c_f32_bf16_e32 v13, v9, v17
	ds_read_b128 v[14:17], v11 offset:5120
	s_waitcnt lgkmcnt(0)
; #define LAS __attribute__((address_space(3)))
; __device__ __forceinline__ float dot2bf(unsigned a, unsigned b, float acc) { return __builtin_amdgcn_fdot2_f32_bf16(__builtin_bit_cast(bf16x2_t, a), __builtin_bit_cast(bf16x2_t, b), acc, false); }
; template <int MODE>
; __device__ __forceinline__ void phase_rowpass1(const Ptrs& P, LAS unsigned char* lds, int layer, int tid_, int vcu, int G) {
;     ...
;             for (int g = 0; g < 16; ++g) { float s = 0.f;
; #pragma unroll
;                 for (int jp = 0; jp < 2; ++jp) { const v4u w = *(const LAS v4u*)(gwt + g * 1024 + 8 * lane + 512 * jp); s = dot2bf(aw[jp].x, w.x, s); s = dot2bf(aw[jp].y, w.y, s); s = dot2bf(aw[jp].z, w.z, s); s = dot2bf(aw[jp].w, w.w, s); }
;                 pg[g] = s; }
	v_dot2c_f32_bf16_e32 v13, v2, v14
	v_mov_b32_e32 v14, v163
	v_dot2c_f32_bf16_e32 v14, v6, v34
	v_dot2c_f32_bf16_e32 v14, v7, v35
	v_dot2c_f32_bf16_e32 v14, v8, v36
	v_dot2c_f32_bf16_e32 v14, v9, v37
	ds_read_b128 v[34:37], v11 offset:7168
	v_dot2c_f32_bf16_e32 v13, v3, v15
	v_mov_b32_e32 v15, v163
	v_dot2c_f32_bf16_e32 v13, v4, v16
	v_mov_b32_e32 v16, v163
	s_waitcnt lgkmcnt(0)
	v_dot2c_f32_bf16_e32 v14, v2, v34
	v_dot2c_f32_bf16_e32 v14, v3, v35
	v_dot2c_f32_bf16_e32 v14, v4, v36
	v_dot2c_f32_bf16_e32 v14, v5, v37
	ds_read_b128 v[34:37], v11 offset:8192
	v_dot2c_f32_bf16_e32 v13, v5, v17
	v_mov_b32_e32 v17, v163
	s_waitcnt lgkmcnt(0)
	v_dot2c_f32_bf16_e32 v15, v6, v34
	v_dot2c_f32_bf16_e32 v15, v7, v35
	v_dot2c_f32_bf16_e32 v15, v8, v36
	v_dot2c_f32_bf16_e32 v15, v9, v37
	ds_read_b128 v[34:37], v11 offset:9216
	s_waitcnt lgkmcnt(0)
	v_dot2c_f32_bf16_e32 v15, v2, v34
	v_dot2c_f32_bf16_e32 v15, v3, v35
	v_dot2c_f32_bf16_e32 v15, v4, v36
	v_dot2c_f32_bf16_e32 v15, v5, v37
	ds_read_b128 v[34:37], v11 offset:10240
	s_waitcnt lgkmcnt(0)
	v_dot2c_f32_bf16_e32 v16, v6, v34
	v_dot2c_f32_bf16_e32 v16, v7, v35
	v_dot2c_f32_bf16_e32 v16, v8, v36
	v_dot2c_f32_bf16_e32 v16, v9, v37
	ds_read_b128 v[34:37], v11 offset:11264
	s_waitcnt lgkmcnt(0)
	v_dot2c_f32_bf16_e32 v16, v2, v34
	v_dot2c_f32_bf16_e32 v16, v3, v35
	v_dot2c_f32_bf16_e32 v16, v4, v36
	v_dot2c_f32_bf16_e32 v16, v5, v37
	ds_read_b128 v[34:37], v11 offset:12288
	s_waitcnt lgkmcnt(0)
	v_dot2c_f32_bf16_e32 v17, v6, v34
	v_dot2c_f32_bf16_e32 v17, v7, v35
	v_dot2c_f32_bf16_e32 v17, v8, v36
	v_dot2c_f32_bf16_e32 v17, v9, v37
	ds_read_b128 v[34:37], v11 offset:13312
	s_waitcnt lgkmcnt(0)
	v_dot2c_f32_bf16_e32 v17, v2, v34
	v_dot2c_f32_bf16_e32 v17, v3, v35
	v_dot2c_f32_bf16_e32 v17, v4, v36
	v_dot2c_f32_bf16_e32 v17, v5, v37
	ds_read_b128 v[34:37], v11 offset:14336
	s_waitcnt lgkmcnt(0)
	v_dot2c_f32_bf16_e32 v19, v6, v34
	v_dot2c_f32_bf16_e32 v19, v7, v35
	v_dot2c_f32_bf16_e32 v19, v8, v36
	v_dot2c_f32_bf16_e32 v19, v9, v37
	ds_read_b128 v[34:37], v11 offset:15360
	s_waitcnt lgkmcnt(0)
	v_dot2c_f32_bf16_e32 v19, v2, v34
	v_dot2c_f32_bf16_e32 v19, v3, v35
	v_dot2c_f32_bf16_e32 v19, v4, v36
	v_dot2c_f32_bf16_e32 v19, v5, v37
	ds_read_b128 v[34:37], v11 offset:16384
	s_waitcnt lgkmcnt(0)
	v_dot2c_f32_bf16_e32 v30, v6, v34
	v_dot2c_f32_bf16_e32 v30, v7, v35
	v_dot2c_f32_bf16_e32 v30, v8, v36
	v_dot2c_f32_bf16_e32 v30, v9, v37
	ds_read_b128 v[34:37], v11 offset:17408
	s_waitcnt lgkmcnt(0)
	v_dot2c_f32_bf16_e32 v30, v2, v34
	v_dot2c_f32_bf16_e32 v30, v3, v35
	v_dot2c_f32_bf16_e32 v30, v4, v36
	v_dot2c_f32_bf16_e32 v30, v5, v37
	ds_read_b128 v[34:37], v11 offset:18432
	s_waitcnt lgkmcnt(0)
	v_dot2c_f32_bf16_e32 v31, v6, v34
	v_dot2c_f32_bf16_e32 v31, v7, v35
	v_dot2c_f32_bf16_e32 v31, v8, v36
	v_dot2c_f32_bf16_e32 v31, v9, v37
	ds_read_b128 v[34:37], v11 offset:19456
	s_waitcnt lgkmcnt(0)
	v_dot2c_f32_bf16_e32 v31, v2, v34
	v_dot2c_f32_bf16_e32 v31, v3, v35
	v_dot2c_f32_bf16_e32 v31, v4, v36
	v_dot2c_f32_bf16_e32 v31, v5, v37
	ds_read_b128 v[34:37], v11 offset:20480
	s_waitcnt lgkmcnt(0)
	v_dot2c_f32_bf16_e32 v33, v6, v34
	v_dot2c_f32_bf16_e32 v33, v7, v35
	v_dot2c_f32_bf16_e32 v33, v8, v36
	v_dot2c_f32_bf16_e32 v33, v9, v37
	ds_read_b128 v[34:37], v11 offset:21504
	s_waitcnt lgkmcnt(0)
	v_dot2c_f32_bf16_e32 v33, v2, v34
	v_dot2c_f32_bf16_e32 v33, v3, v35
	v_dot2c_f32_bf16_e32 v33, v4, v36
	v_dot2c_f32_bf16_e32 v33, v5, v37
	ds_read_b128 v[34:37], v11 offset:22528
	s_waitcnt lgkmcnt(0)
	v_dot2c_f32_bf16_e32 v38, v6, v34
	v_dot2c_f32_bf16_e32 v38, v7, v35
	v_dot2c_f32_bf16_e32 v38, v8, v36
	v_dot2c_f32_bf16_e32 v38, v9, v37
	ds_read_b128 v[34:37], v11 offset:23552
	s_waitcnt lgkmcnt(0)
	v_dot2c_f32_bf16_e32 v38, v2, v34
	v_dot2c_f32_bf16_e32 v38, v3, v35
	v_dot2c_f32_bf16_e32 v38, v4, v36
	v_dot2c_f32_bf16_e32 v38, v5, v37
	ds_read_b128 v[34:37], v11 offset:24576
	s_waitcnt lgkmcnt(0)
	v_dot2c_f32_bf16_e32 v39, v6, v34
	v_dot2c_f32_bf16_e32 v39, v7, v35
	v_dot2c_f32_bf16_e32 v39, v8, v36
	v_dot2c_f32_bf16_e32 v39, v9, v37
	ds_read_b128 v[34:37], v11 offset:25600
	s_waitcnt lgkmcnt(0)
	v_dot2c_f32_bf16_e32 v39, v2, v34
	v_dot2c_f32_bf16_e32 v39, v3, v35
	v_dot2c_f32_bf16_e32 v39, v4, v36
	v_dot2c_f32_bf16_e32 v39, v5, v37
	ds_read_b128 v[34:37], v11 offset:26624
	s_waitcnt lgkmcnt(0)
	v_dot2c_f32_bf16_e32 v40, v6, v34
	v_dot2c_f32_bf16_e32 v40, v7, v35
	v_dot2c_f32_bf16_e32 v40, v8, v36
	v_dot2c_f32_bf16_e32 v40, v9, v37
	ds_read_b128 v[34:37], v11 offset:27648
	s_waitcnt lgkmcnt(0)
	v_dot2c_f32_bf16_e32 v40, v2, v34
	v_dot2c_f32_bf16_e32 v40, v3, v35
	v_dot2c_f32_bf16_e32 v40, v4, v36
	v_dot2c_f32_bf16_e32 v40, v5, v37
	ds_read_b128 v[34:37], v11 offset:28672
	s_waitcnt lgkmcnt(0)
	v_dot2c_f32_bf16_e32 v41, v6, v34
	v_dot2c_f32_bf16_e32 v41, v7, v35
	v_dot2c_f32_bf16_e32 v41, v8, v36
	v_dot2c_f32_bf16_e32 v41, v9, v37
	ds_read_b128 v[34:37], v11 offset:29696
	s_waitcnt lgkmcnt(0)
; #define LAS __attribute__((address_space(3)))
; __device__ __forceinline__ float logsigf_(float x) { return fminf(x, 0.f) - __logf(1.f + __expf(-fabsf(x))); }
; #define SHX(v, m) (((m) < 32) ? __int_as_float(__builtin_amdgcn_ds_swizzle(__float_as_int(v), ((((m) & 31) << 10) | 0x1f))) : shx32(v))
; __device__ __forceinline__ float dot2bf(unsigned a, unsigned b, float acc) { return __builtin_amdgcn_fdot2_f32_bf16(__builtin_bit_cast(bf16x2_t, a), __builtin_bit_cast(bf16x2_t, b), acc, false); }
; template <int MODE>
; __device__ __forceinline__ void phase_rowpass1(const Ptrs& P, LAS unsigned char* lds, int layer, int tid_, int vcu, int G) {
;     ...
;             for (int g = 0; g < 16; ++g) { float s = 0.f;
; #pragma unroll
;                 for (int jp = 0; jp < 2; ++jp) { const v4u w = *(const LAS v4u*)(gwt + g * 1024 + 8 * lane + 512 * jp); s = dot2bf(aw[jp].x, w.x, s); s = dot2bf(aw[jp].y, w.y, s); s = dot2bf(aw[jp].z, w.z, s); s = dot2bf(aw[jp].w, w.w, s); }
;                 pg[g] = s; }
;             float p8[8], p4[4], p2[2], p1;
;             { const bool hi = (lane & 32) != 0;
; #pragma unroll
;               for (int i = 0; i < 8; ++i) { const float send = hi ? pg[i] : pg[8 + i], keep = hi ? pg[8 + i] : pg[i]; p8[i] = keep + SHX(send, 32); } }
;             { const bool hi = (lane & 16) != 0;
; #pragma unroll
;               for (int i = 0; i < 4; ++i) { const float send = hi ? p8[i] : p8[4 + i], keep = hi ? p8[4 + i] : p8[i]; p4[i] = keep + SHX(send, 16); } }
;             { const bool hi = (lane & 8) != 0;
; #pragma unroll
;               for (int i = 0; i < 2; ++i) { const float send = hi ? p4[i] : p4[2 + i], keep = hi ? p4[2 + i] : p4[i]; p2[i] = keep + SHX(send, 8); } }
;             { const bool hi = (lane & 4) != 0; const float send = hi ? p2[0] : p2[1], keep = hi ? p2[1] : p2[0]; p1 = keep + SHX(send, 4); }
;             p1 += SHX(p1, 2); p1 += SHX(p1, 1);
;             const int src = (((lane >> 3) & 1) << 5) | (((lane >> 2) & 1) << 4) | (((lane >> 1) & 1) << 3) | ((lane & 1) << 2);
;             const float mine = __int_as_float(__builtin_amdgcn_ds_bpermute(src << 2, __float_as_int(p1)));
;             if (lane < 16) { float gv = mine + P.gate_b[layer * 16 + lane]; if ((lane >> 2) & 1) gv = logsigf_(gv); ((float*)(P.ws + WS_GATES))[(size_t)row * 16 + lane] = gv; }
	v_dot2c_f32_bf16_e32 v41, v2, v34
	v_dot2c_f32_bf16_e32 v41, v3, v35
	v_dot2c_f32_bf16_e32 v41, v4, v36
	v_dot2c_f32_bf16_e32 v41, v5, v37
	ds_read_b128 v[34:37], v11 offset:30720
	s_waitcnt lgkmcnt(0)
	v_dot2c_f32_bf16_e32 v42, v6, v34
	v_dot2c_f32_bf16_e32 v42, v7, v35
	v_dot2c_f32_bf16_e32 v42, v8, v36
	v_dot2c_f32_bf16_e32 v42, v9, v37
	ds_read_b128 v[6:9], v11 offset:31744
	s_waitcnt lgkmcnt(0)
	v_dot2c_f32_bf16_e32 v42, v2, v6
	v_dot2c_f32_bf16_e32 v42, v3, v7
	v_dot2c_f32_bf16_e32 v42, v4, v8
	v_mbcnt_lo_u32_b32 v4, -1, 0
	v_cndmask_b32_e32 v2, v10, v30, vcc
	v_mbcnt_hi_u32_b32 v4, -1, v4
	v_dot2c_f32_bf16_e32 v42, v5, v9
	v_lshlrev_b32_e32 v4, 2, v4
	v_xor_b32_e32 v4, 0x80, v4
	ds_bpermute_b32 v2, v4, v2
	v_mbcnt_lo_u32_b32 v5, -1, 0
	v_cndmask_b32_e32 v3, v30, v10, vcc
	v_mbcnt_hi_u32_b32 v5, -1, v5
	v_mbcnt_lo_u32_b32 v6, -1, 0
	s_waitcnt lgkmcnt(0)
	v_add_f32_e32 v2, v3, v2
	v_lshlrev_b32_e32 v5, 2, v5
	v_cndmask_b32_e32 v3, v12, v31, vcc
	v_xor_b32_e32 v5, 0x80, v5
	ds_bpermute_b32 v3, v5, v3
	v_mbcnt_hi_u32_b32 v6, -1, v6
	v_cndmask_b32_e32 v4, v31, v12, vcc
	v_lshlrev_b32_e32 v6, 2, v6
	v_xor_b32_e32 v6, 0x80, v6
	s_waitcnt lgkmcnt(0)
	v_add_f32_e32 v3, v4, v3
	v_cndmask_b32_e32 v4, v13, v33, vcc
	ds_bpermute_b32 v4, v6, v4
	v_mbcnt_lo_u32_b32 v7, -1, 0
	v_cndmask_b32_e32 v5, v33, v13, vcc
	v_mbcnt_hi_u32_b32 v7, -1, v7
	v_mbcnt_lo_u32_b32 v8, -1, 0
	s_waitcnt lgkmcnt(0)
	v_add_f32_e32 v4, v5, v4
	v_lshlrev_b32_e32 v7, 2, v7
	v_cndmask_b32_e32 v5, v14, v38, vcc
	v_xor_b32_e32 v7, 0x80, v7
	ds_bpermute_b32 v5, v7, v5
	v_mbcnt_hi_u32_b32 v8, -1, v8
	v_cndmask_b32_e32 v6, v38, v14, vcc
	v_lshlrev_b32_e32 v8, 2, v8
	v_xor_b32_e32 v8, 0x80, v8
	s_waitcnt lgkmcnt(0)
	v_add_f32_e32 v5, v6, v5
	v_cndmask_b32_e32 v6, v15, v39, vcc
	ds_bpermute_b32 v6, v8, v6
	v_mbcnt_lo_u32_b32 v9, -1, 0
	v_cndmask_b32_e32 v7, v39, v15, vcc
	v_mbcnt_hi_u32_b32 v9, -1, v9
	v_mbcnt_lo_u32_b32 v10, -1, 0
	s_waitcnt lgkmcnt(0)
	v_add_f32_e32 v6, v7, v6
	v_lshlrev_b32_e32 v9, 2, v9
	v_cndmask_b32_e32 v7, v16, v40, vcc
	v_xor_b32_e32 v9, 0x80, v9
	ds_bpermute_b32 v7, v9, v7
	v_mbcnt_hi_u32_b32 v10, -1, v10
	v_cndmask_b32_e32 v8, v40, v16, vcc
	v_lshlrev_b32_e32 v10, 2, v10
	v_xor_b32_e32 v10, 0x80, v10
	s_waitcnt lgkmcnt(0)
	v_add_f32_e32 v7, v8, v7
	v_cndmask_b32_e32 v8, v17, v41, vcc
	ds_bpermute_b32 v8, v10, v8
	v_mbcnt_lo_u32_b32 v11, -1, 0
	v_cndmask_b32_e32 v9, v41, v17, vcc
	v_mbcnt_hi_u32_b32 v11, -1, v11
	v_cndmask_b32_e32 v10, v42, v19, vcc
	v_lshlrev_b32_e32 v11, 2, v11
	s_waitcnt lgkmcnt(0)
	v_add_f32_e32 v8, v9, v8
	v_cndmask_b32_e32 v9, v19, v42, vcc
	v_xor_b32_e32 v11, 0x80, v11
	ds_bpermute_b32 v9, v11, v9
	s_waitcnt lgkmcnt(0)
	v_add_f32_e32 v9, v10, v9
	v_cndmask_b32_e64 v10, v2, v6, s[38:39]
	v_cndmask_b32_e64 v2, v6, v2, s[38:39]
	ds_swizzle_b32 v6, v10 offset:swizzle(SWAP,16)
	s_waitcnt lgkmcnt(0)
	v_add_f32_e32 v2, v2, v6
	v_cndmask_b32_e64 v6, v3, v7, s[38:39]
	ds_swizzle_b32 v6, v6 offset:swizzle(SWAP,16)
	v_cndmask_b32_e64 v3, v7, v3, s[38:39]
	s_waitcnt lgkmcnt(0)
	v_add_f32_e32 v3, v3, v6
	v_cndmask_b32_e64 v6, v4, v8, s[38:39]
	ds_swizzle_b32 v6, v6 offset:swizzle(SWAP,16)
	v_cndmask_b32_e64 v4, v8, v4, s[38:39]
	s_waitcnt lgkmcnt(0)
	v_add_f32_e32 v4, v4, v6
	v_cndmask_b32_e64 v6, v5, v9, s[38:39]
	ds_swizzle_b32 v6, v6 offset:swizzle(SWAP,16)
	v_cndmask_b32_e64 v5, v9, v5, s[38:39]
	s_waitcnt lgkmcnt(0)
	v_add_f32_e32 v5, v5, v6
	v_cndmask_b32_e64 v6, v2, v4, s[40:41]
	v_cndmask_b32_e64 v2, v4, v2, s[40:41]
	ds_swizzle_b32 v4, v6 offset:swizzle(SWAP,8)
	s_waitcnt lgkmcnt(0)
	v_add_f32_e32 v2, v2, v4
	v_cndmask_b32_e64 v4, v3, v5, s[40:41]
	ds_swizzle_b32 v4, v4 offset:swizzle(SWAP,8)
	v_cndmask_b32_e64 v3, v5, v3, s[40:41]
	s_waitcnt lgkmcnt(0)
	v_add_f32_e32 v3, v3, v4
	v_cndmask_b32_e64 v4, v2, v3, s[42:43]
	v_cndmask_b32_e64 v2, v3, v2, s[42:43]
	ds_swizzle_b32 v3, v4 offset:swizzle(SWAP,4)
	s_waitcnt lgkmcnt(0)
	v_add_f32_e32 v2, v2, v3
	ds_swizzle_b32 v3, v2 offset:swizzle(SWAP,2)
	s_waitcnt lgkmcnt(0)
	v_add_f32_e32 v2, v2, v3
	s_waitcnt lgkmcnt(0)
	s_nop 1
	v_add_f32_dpp v2, v2, v2 quad_perm:[1,0,3,2] row_mask:0xf bank_mask:0xf
	ds_bpermute_b32 v2, v32, v2
	s_and_saveexec_b64 s[8:9], s[44:45]
	s_cbranch_execz .LBB0_278
	global_load_dword v3, v[22:23], off
	s_waitcnt vmcnt(0) lgkmcnt(0)
	v_add_f32_e32 v2, v3, v2
	s_and_saveexec_b64 s[18:19], s[46:47]
	s_cbranch_execz .LBB0_277
	s_mov_b32 s4, 0xbfb8aa3b
	v_mul_f32_e64 v3, |v2|, s4
	v_exp_f32_e32 v3, v3
	s_mov_b32 s4, 0x3f317217
	v_max_f32_e32 v2, v2, v2
	v_min_f32_e32 v2, 0, v2
	v_add_f32_e32 v3, 1.0, v3
	v_cmp_gt_f32_e64 s[48:49], s73, v3
	s_nop 1
	v_cndmask_b32_e64 v4, 0, 32, s[48:49]
	v_ldexp_f32 v3, v3, v4
	v_log_f32_e32 v3, v3
	s_nop 0
	v_mul_f32_e32 v4, 0x3f317217, v3
	v_fma_f32 v4, v3, s4, -v4
	v_fmac_f32_e32 v4, 0x3377d1cf, v3
	s_mov_b32 s4, 0x7f800000
	v_fmac_f32_e32 v4, 0x3f317217, v3
	v_cmp_lt_f32_e64 s[50:51], |v3|, s4
	s_nop 1
	v_cndmask_b32_e64 v3, v3, v4, s[50:51]
	v_cndmask_b32_e64 v4, 0, v247, s[48:49]
	v_sub_f32_e32 v3, v3, v4
	v_sub_f32_e32 v2, v2, v3
	s_branch .LBB0_277

; __device__ __forceinline__ unsigned pk2(float lo, float hi) { unsigned r; asm("v_cvt_pk_bf16_f32 %0, %1, %2" : "=v"(r) : "v"(lo), "v"(hi)); return r; }
; __device__ __forceinline__ float bflo(unsigned w) { return __uint_as_float(w << 16); }
; __device__ __forceinline__ float bfhi(unsigned w) { return __uint_as_float(w & 0xffff0000u); }
; __device__ __forceinline__ void phase_rowpass2(const Ptrs& P, int layer, int tid_, int vcu, int G) {
;     ...
;     for (int row = gw; row < T; row += NGW) {
;         f32x4 v[4]; float ss = 0.f;
; #pragma unroll
;         for (int jp = 0; jp < 2; ++jp) { const v4u hw = ((const v4u*)(H + (size_t)row * D))[lane + 64 * jp];
;             v[2 * jp] = (f32x4){bflo(hw.x), bfhi(hw.x), bflo(hw.y), bfhi(hw.y)}; v[2 * jp + 1] = (f32x4){bflo(hw.z), bfhi(hw.z), bflo(hw.w), bfhi(hw.w)}; }
; #pragma unroll
;         for (int j = 0; j < 4; ++j) ss += v[j][0] * v[j][0] + v[j][1] * v[j][1] + v[j][2] * v[j][2] + v[j][3] * v[j][3];
;         const float rstd = rsqrtf(wave_sum(ss) * (1.f / D) + EPS);
;         bf16* A = (bf16*)(P.ws + WS_XM) + (size_t)row * D;
; #pragma unroll
;         for (int jp = 0; jp < 2; ++jp) { float x[8];
; #pragma unroll
;             for (int h = 0; h < 2; ++h) { const f32x4 g = ((const f32x4*)g2)[F4(2 * jp + h)];
; #pragma unroll
;                 for (int i = 0; i < 4; ++i) x[4 * h + i] = v[2 * jp + h][i] * rstd * g[i]; }
;             v4u w; w.x = pk2(x[0], x[1]); w.y = pk2(x[2], x[3]); w.z = pk2(x[4], x[5]); w.w = pk2(x[6], x[7]); ((v4u*)A)[lane + 64 * jp] = w;
;             v2u w8; w8.x = (unsigned)__builtin_amdgcn_cvt_pk_fp8_f32(x[2] * SX8, x[3] * SX8, __builtin_amdgcn_cvt_pk_fp8_f32(x[0] * SX8, x[1] * SX8, 0, false), true);
;             w8.y = (unsigned)__builtin_amdgcn_cvt_pk_fp8_f32(x[6] * SX8, x[7] * SX8, __builtin_amdgcn_cvt_pk_fp8_f32(x[4] * SX8, x[5] * SX8, 0, false), true);
;             ((v2u*)(P.ws + WS_XM8 + (size_t)row * D))[lane + 64 * jp] = w8; }
;     }
.LBB0_985:
	v_lshl_add_u64 v[28:29], s[6:7], 0, v[6:7]
	v_add_co_u32_e32 v12, vcc, 0x34600000, v28
	s_mov_b32 s4, 0x6a200000
	s_nop 0
	v_addc_co_u32_e32 v13, vcc, 0, v29, vcc
	global_load_dwordx4 v[8:11], v[12:13], off
	global_load_dwordx4 v[16:19], v[12:13], off offset:1024
	v_add_u32_e32 v1, s74, v1
	v_lshl_add_u64 v[6:7], v[6:7], 0, s[94:95]
	s_waitcnt vmcnt(1)
	v_and_b32_e32 v31, 0xffff0000, v10
	v_and_b32_e32 v30, 0xffff0000, v8
	v_lshlrev_b32_e32 v21, 16, v10
	v_lshlrev_b32_e32 v20, 16, v8
	v_lshlrev_b32_e32 v32, 16, v9
	v_and_b32_e32 v34, 0xffff0000, v9
	v_pk_mul_f32 v[8:9], v[30:31], v[30:31]
	v_lshlrev_b32_e32 v33, 16, v11
	v_pk_fma_f32 v[8:9], v[20:21], v[20:21], v[8:9]
	v_and_b32_e32 v35, 0xffff0000, v11
	v_pk_fma_f32 v[8:9], v[32:33], v[32:33], v[8:9]
	s_waitcnt vmcnt(0)
	v_lshlrev_b32_e32 v15, 16, v16
	v_pk_fma_f32 v[22:23], v[34:35], v[34:35], v[8:9]
	v_and_b32_e32 v9, 0xffff0000, v16
	v_and_b32_e32 v8, 0xffff0000, v18
	v_lshlrev_b32_e32 v14, 16, v18
	v_lshlrev_b32_e32 v13, 16, v17
	v_and_b32_e32 v11, 0xffff0000, v17
	v_pk_mul_f32 v[16:17], v[8:9], v[8:9]
	v_lshlrev_b32_e32 v12, 16, v19
	v_pk_fma_f32 v[16:17], v[14:15], v[14:15], v[16:17]
	v_and_b32_e32 v10, 0xffff0000, v19
	v_pk_fma_f32 v[16:17], v[12:13], v[12:13], v[16:17]
	v_add_f32_e32 v18, v22, v23
	v_pk_fma_f32 v[16:17], v[10:11], v[10:11], v[16:17]
	s_nop 0
	v_add_f32_e32 v17, v18, v17
	v_add_f32_e32 v16, v16, v17
	s_waitcnt lgkmcnt(0)
	s_nop 1
	v_add_f32_dpp v16, v16, v16 quad_perm:[1,0,3,2] row_mask:0xf bank_mask:0xf
	s_waitcnt lgkmcnt(0)
	s_nop 1
	v_add_f32_dpp v16, v16, v16 quad_perm:[2,3,0,1] row_mask:0xf bank_mask:0xf
	s_waitcnt lgkmcnt(0)
	s_nop 1
	v_add_f32_dpp v16, v16, v16 row_half_mirror row_mask:0xf bank_mask:0xf
	s_waitcnt lgkmcnt(0)
	s_nop 1
	v_add_f32_dpp v16, v16, v16 row_mirror row_mask:0xf bank_mask:0xf
	ds_swizzle_b32 v17, v16 offset:swizzle(SWAP,16)
	s_waitcnt lgkmcnt(0)
	v_add_f32_e32 v16, v16, v17
	v_mbcnt_lo_u32_b32 v17, -1, 0
	s_nop 0
	v_mbcnt_hi_u32_b32 v17, -1, v17
	s_nop 0
	v_lshlrev_b32_e32 v17, 2, v17
	v_xor_b32_e32 v17, 0x80, v17
	ds_bpermute_b32 v17, v17, v16
	s_waitcnt lgkmcnt(0)
	v_add_f32_e32 v16, v16, v17
	v_fmamk_f32 v16, v16, 0x3a800000, v196
	v_cmp_gt_f32_e32 vcc, s73, v16
	v_mul_f32_e32 v17, 0x4b800000, v16
	s_nop 0
	v_cndmask_b32_e32 v16, v16, v17, vcc
	v_rsq_f32_e32 v16, v16
	s_nop 0
	v_mul_f32_e32 v17, 0x45800000, v16
	v_cndmask_b32_e32 v22, v16, v17, vcc
	global_load_dwordx4 v[16:19], v[2:3], off offset:16
	global_load_dwordx4 v[24:27], v[2:3], off
	v_mul_f32_e32 v20, v22, v20
	v_mul_f32_e32 v9, v22, v9
	v_mul_f32_e32 v8, v22, v8
	v_mul_f32_e32 v15, v22, v15
	s_waitcnt vmcnt(0)
	v_mul_f32_e32 v23, v24, v20
	v_mul_f32_e32 v20, v22, v30
	v_mul_f32_e32 v24, v25, v20
	v_mul_f32_e32 v20, v22, v32
	v_mul_f32_e32 v25, v26, v20
	v_mul_f32_e32 v20, v22, v34
	v_mul_f32_e32 v26, v27, v20
	v_mul_f32_e32 v20, v22, v21
	v_mul_f32_e32 v27, v16, v20
	v_mul_f32_e32 v16, v22, v31
	v_mul_f32_e32 v30, v17, v16
	v_mul_f32_e32 v16, v22, v33
	v_mul_f32_e32 v31, v18, v16
	v_mul_f32_e32 v16, v22, v35
	v_mul_f32_e32 v32, v19, v16
	v_add_co_u32_e32 v16, vcc, s25, v28
	v_cvt_pk_bf16_f32 v20, v27, v30
	v_cvt_pk_bf16_f32 v21, v31, v32
	v_cvt_pk_bf16_f32 v18, v23, v24
	v_cvt_pk_bf16_f32 v19, v25, v26
	s_nop 1
	v_addc_co_u32_e32 v17, vcc, 0, v29, vcc
	global_store_dwordx4 v[16:17], v[18:21], off
	s_nop 1
	v_mul_f32_e32 v21, 0x41000000, v23
	v_mul_f32_e32 v23, 0x41000000, v24
	v_mov_b32_e32 v20, v163
	v_cvt_pk_fp8_f32 v20, v21, v23
	v_mul_f32_e32 v23, 0x41000000, v27
	v_mul_f32_e32 v24, 0x41000000, v30
	v_mov_b32_e32 v21, v163
	v_cvt_pk_fp8_f32 v21, v23, v24
	v_mul_f32_e32 v18, 0x41000000, v25
	v_mul_f32_e32 v19, 0x41000000, v26
	v_cvt_pk_fp8_f32 v20, v18, v19 op_sel:[0,0,1]
	v_mul_f32_e32 v18, 0x41000000, v31
	v_mul_f32_e32 v19, 0x41000000, v32
	v_cvt_pk_fp8_f32 v21, v18, v19 op_sel:[0,0,1]
	v_lshl_add_u64 v[18:19], s[6:7], 0, v[4:5]
	v_add_co_u32_e32 v18, vcc, s4, v18
	v_lshl_add_u64 v[4:5], v[4:5], 0, s[10:11]
	s_nop 0
	v_addc_co_u32_e32 v19, vcc, 0, v19, vcc
	global_store_dwordx2 v[18:19], v[20:21], off
	global_load_dwordx4 v[24:27], v[2:3], off offset:2064
	global_load_dwordx4 v[28:31], v[2:3], off offset:2048
	v_cmp_lt_i32_e32 vcc, s9, v1
	s_or_b64 s[12:13], vcc, s[12:13]
	s_waitcnt vmcnt(1)
	v_mul_f32_e32 v23, v25, v8
	s_waitcnt vmcnt(0)
	v_mul_f32_e32 v20, v29, v9
	v_mul_f32_e32 v9, v22, v13
	v_mul_f32_e32 v13, v30, v9
	v_mul_f32_e32 v9, v22, v11
	v_mul_f32_e32 v8, v22, v12
	v_mul_f32_e32 v21, v31, v9
	v_mul_f32_e32 v9, v22, v14
	v_mul_f32_e32 v12, v26, v8
	v_mul_f32_e32 v8, v22, v10
	v_mul_f32_e32 v15, v28, v15
	v_mul_f32_e32 v14, v24, v9
	v_mul_f32_e32 v22, v27, v8
	v_cvt_pk_bf16_f32 v8, v15, v20
	v_cvt_pk_bf16_f32 v9, v13, v21
	v_cvt_pk_bf16_f32 v11, v12, v22
	v_cvt_pk_bf16_f32 v10, v14, v23
	global_store_dwordx4 v[16:17], v[8:11], off offset:1024
	s_nop 1
	v_mul_f32_e32 v9, 0x41000000, v13
	v_mul_f32_e32 v11, 0x41000000, v15
	v_mul_f32_e32 v13, 0x41000000, v20
	v_mov_b32_e32 v8, v163
	v_cvt_pk_fp8_f32 v8, v11, v13
	v_mul_f32_e32 v10, 0x41000000, v21
	v_mul_f32_e32 v13, 0x41000000, v23
	v_mul_f32_e32 v11, 0x41000000, v22
	v_cvt_pk_fp8_f32 v8, v9, v10 op_sel:[0,0,1]
	v_mul_f32_e32 v10, 0x41000000, v12
	v_mul_f32_e32 v12, 0x41000000, v14
	v_mov_b32_e32 v9, v163
	v_cvt_pk_fp8_f32 v9, v12, v13
	v_cvt_pk_fp8_f32 v9, v10, v11 op_sel:[0,0,1]
	global_store_dwordx2 v[18:19], v[8:9], off offset:512
	s_andn2_b64 exec, exec, s[12:13]
	s_cbranch_execnz .LBB0_985

; __device__ __forceinline__ float bflo(unsigned w) { return __uint_as_float(w << 16); }
; __device__ __forceinline__ float bfhi(unsigned w) { return __uint_as_float(w & 0xffff0000u); }
; #define SHX(v, m) (((m) < 32) ? __int_as_float(__builtin_amdgcn_ds_swizzle(__float_as_int(v), ((((m) & 31) << 10) | 0x1f))) : shx32(v))
; __device__ __forceinline__ float wave_sum(float v) {
;     v += SHX(v, 1); v += SHX(v, 2); v += SHX(v, 4); v += SHX(v, 8); v += SHX(v, 16); v += SHX(v, 32);
;     return v;
; template <int MODE>
; __device__ __forceinline__ void phase_rowpass1(const Ptrs& P, LAS unsigned char* lds, int layer, int tid_, int vcu, int G) {
;     ...
;             f32x4 e[4]; float ss = 0.f;
; #pragma unroll
;             for (int jp = 0; jp < 2; ++jp) { const v4u hw = ((const v4u*)(H + (size_t)row * D))[lane + 64 * jp]; const v4u w = __builtin_nontemporal_load((const v4u*)(GE + (size_t)row * D) + lane + 64 * jp);
;                 v[2 * jp] = (f32x4){bflo(hw.x), bfhi(hw.x), bflo(hw.y), bfhi(hw.y)}; v[2 * jp + 1] = (f32x4){bflo(hw.z), bfhi(hw.z), bflo(hw.w), bfhi(hw.w)};
;                 e[2 * jp] = (f32x4){bflo(w.x), bfhi(w.x), bflo(w.y), bfhi(w.y)}; e[2 * jp + 1] = (f32x4){bflo(w.z), bfhi(w.z), bflo(w.w), bfhi(w.w)}; }
; #pragma unroll
;             for (int j = 0; j < 4; ++j) ss += e[j][0] * e[j][0] + e[j][1] * e[j][1] + e[j][2] * e[j][2] + e[j][3] * e[j][3];
;             const float r = rsqrtf(wave_sum(ss) * (1.f / D) + EPS);
; #pragma unroll
;             for (int j = 0; j < 4; ++j) { const f32x4 g = ((const f32x4*)pg)[F4(j)]; v[j] = v[j] + e[j] * r * g; }
.LBB0_1574:
	v_add_co_u32_e32 v18, vcc, 0x31400000, v14
	global_load_dwordx4 v[0:3], v[14:15], off
	global_load_dwordx4 v[4:7], v[14:15], off offset:1024
	v_addc_co_u32_e32 v19, vcc, 0, v15, vcc
	global_load_dwordx4 v[22:25], v[18:19], off nt
	global_load_dwordx4 v[26:29], v[18:19], off offset:1024 nt
	v_mbcnt_lo_u32_b32 v18, -1, 0
	v_add_u32_e32 v20, s74, v20
	v_mbcnt_hi_u32_b32 v18, -1, v18
	global_load_dwordx4 v[30:33], v[8:9], off offset:16
	global_load_dwordx4 v[34:37], v[8:9], off
	global_load_dwordx4 v[38:41], v[10:11], off offset:16
	global_load_dwordx4 v[42:45], v[10:11], off
	v_mbcnt_lo_u32_b32 v19, -1, 0
	v_lshlrev_b32_e32 v18, 2, v18
	v_mbcnt_hi_u32_b32 v19, -1, v19
	global_load_dwordx4 v[46:49], v[12:13], off offset:16
	global_load_dwordx4 v[50:53], v[12:13], off
	global_load_dwordx4 v[54:57], v[12:13], off offset:2064
	global_load_dwordx4 v[58:61], v[12:13], off offset:2048
	v_xor_b32_e32 v88, 0x80, v18
	v_cmp_lt_i32_e32 vcc, s3, v20
	s_or_b64 s[0:1], vcc, s[0:1]
	v_lshlrev_b32_e32 v18, 2, v19
	v_xor_b32_e32 v89, 0x80, v18
	v_lshl_add_u64 v[14:15], v[14:15], 0, s[94:95]
	s_waitcnt vmcnt(11)
	v_lshlrev_b32_e32 v18, 16, v0
	v_and_b32_e32 v19, 0xffff0000, v0
	v_lshlrev_b32_e32 v62, 16, v2
	s_waitcnt vmcnt(9)
	v_and_b32_e32 v71, 0xffff0000, v24
	v_and_b32_e32 v70, 0xffff0000, v22
	v_lshlrev_b32_e32 v69, 16, v24
	v_lshlrev_b32_e32 v68, 16, v22
	v_lshlrev_b32_e32 v72, 16, v23
	v_and_b32_e32 v24, 0xffff0000, v23
	s_waitcnt vmcnt(8)
	v_lshlrev_b32_e32 v23, 16, v26
	v_lshlrev_b32_e32 v22, 16, v28
	v_and_b32_e32 v75, 0xffff0000, v26
	v_and_b32_e32 v74, 0xffff0000, v28
	v_lshlrev_b32_e32 v76, 16, v29
	v_and_b32_e32 v26, 0xffff0000, v29
	v_pk_mul_f32 v[28:29], v[70:71], v[70:71]
	v_lshlrev_b32_e32 v73, 16, v25
	v_pk_mul_f32 v[78:79], v[74:75], v[74:75]
	v_pk_fma_f32 v[28:29], v[68:69], v[68:69], v[28:29]
	v_and_b32_e32 v25, 0xffff0000, v25
	v_lshlrev_b32_e32 v77, 16, v27
	v_mov_b32_e32 v80, v68
	v_mov_b32_e32 v81, v70
	v_mov_b32_e32 v70, v69
	v_pk_fma_f32 v[68:69], v[22:23], v[22:23], v[78:79]
	v_pk_fma_f32 v[28:29], v[72:73], v[72:73], v[28:29]
	v_and_b32_e32 v27, 0xffff0000, v27
	v_pk_fma_f32 v[68:69], v[76:77], v[76:77], v[68:69]
	v_pk_fma_f32 v[28:29], v[24:25], v[24:25], v[28:29]
	v_mov_b32_e32 v86, v77
	v_mov_b32_e32 v87, v27
	v_mov_b32_e32 v77, v26
	v_pk_fma_f32 v[26:27], v[26:27], v[26:27], v[68:69]
	v_add_f32_e32 v28, v28, v29
	v_add_f32_e32 v27, v28, v27
	v_add_f32_e32 v26, v26, v27
	v_mov_b32_e32 v83, v24
	v_mov_b32_e32 v24, v73
	v_and_b32_e32 v63, 0xffff0000, v2
	v_lshlrev_b32_e32 v2, 16, v3
	s_waitcnt lgkmcnt(0)
	s_nop 1
	v_add_f32_dpp v26, v26, v26 quad_perm:[1,0,3,2] row_mask:0xf bank_mask:0xf
	v_and_b32_e32 v3, 0xffff0000, v3
	v_mov_b32_e32 v84, v23
	v_mov_b32_e32 v85, v75
	v_mov_b32_e32 v23, v74
	s_waitcnt lgkmcnt(0)
	s_nop 1
	v_add_f32_dpp v26, v26, v26 quad_perm:[2,3,0,1] row_mask:0xf bank_mask:0xf
	v_lshlrev_b32_e32 v64, 16, v4
	v_and_b32_e32 v65, 0xffff0000, v4
	v_lshlrev_b32_e32 v66, 16, v6
	v_and_b32_e32 v67, 0xffff0000, v6
	s_waitcnt lgkmcnt(0)
	s_nop 1
	v_add_f32_dpp v26, v26, v26 row_half_mirror row_mask:0xf bank_mask:0xf
	v_mov_b32_e32 v82, v72
	v_lshlrev_b32_e32 v0, 16, v1
	v_and_b32_e32 v1, 0xffff0000, v1
	v_lshlrev_b32_e32 v6, 16, v7
	s_waitcnt lgkmcnt(0)
	s_nop 1
	v_add_f32_dpp v26, v26, v26 row_mirror row_mask:0xf bank_mask:0xf
	ds_swizzle_b32 v27, v26 offset:swizzle(SWAP,16)
	v_and_b32_e32 v7, 0xffff0000, v7
	v_lshlrev_b32_e32 v4, 16, v5
	v_and_b32_e32 v5, 0xffff0000, v5
	s_waitcnt lgkmcnt(0)
	v_add_f32_e32 v26, v26, v27
	ds_bpermute_b32 v27, v88, v26
	s_waitcnt lgkmcnt(0)
; __device__ __forceinline__ unsigned pk2(float lo, float hi) { unsigned r; asm("v_cvt_pk_bf16_f32 %0, %1, %2" : "=v"(r) : "v"(lo), "v"(hi)); return r; }
; template <int MODE>
; __device__ __forceinline__ void phase_rowpass1(const Ptrs& P, LAS unsigned char* lds, int layer, int tid_, int vcu, int G) {
;     ...
;             const float r = rsqrtf(wave_sum(ss) * (1.f / D) + EPS);
; #pragma unroll
;             for (int j = 0; j < 4; ++j) { const f32x4 g = ((const f32x4*)pg)[F4(j)]; v[j] = v[j] + e[j] * r * g; }
;         }
;         if (MODE != 2) {
; #pragma unroll
;             for (int jp = 0; jp < 2; ++jp) { v4u hw; hw.x = pk2(v[2 * jp][0], v[2 * jp][1]); hw.y = pk2(v[2 * jp][2], v[2 * jp][3]); hw.z = pk2(v[2 * jp + 1][0], v[2 * jp + 1][1]); hw.w = pk2(v[2 * jp + 1][2], v[2 * jp + 1][3]);
;                 ((v4u*)(H + (size_t)row * D))[lane + 64 * jp] = hw; }
;         }
;         float ss = 0.f;
; #pragma unroll
;         for (int j = 0; j < 4; ++j) ss += v[j][0] * v[j][0] + v[j][1] * v[j][1] + v[j][2] * v[j][2] + v[j][3] * v[j][3];
;         const float rstd = rsqrtf(wave_sum(ss) * (1.f / D) + EPS);
; #pragma unroll
;         for (int j = 0; j < 4; ++j) { const f32x4 g = ((const f32x4*)g1)[F4(j)]; v[j] = v[j] * rstd * g; }
;         if (MODE == 2) {
; #pragma unroll
;             for (int j = 0; j < 4; ++j) ((f32x4*)(P.out + (size_t)row * D))[F4(j)] = v[j];
	v_add_f32_e32 v26, v26, v27
	v_fmamk_f32 v26, v26, 0x3a800000, v21
	v_mul_f32_e32 v27, 0x4b800000, v26
	v_cmp_gt_f32_e32 vcc, s2, v26
	s_nop 1
	v_cndmask_b32_e32 v26, v26, v27, vcc
	v_rsq_f32_e32 v26, v26
	s_nop 0
	v_mul_f32_e32 v27, 0x45800000, v26
	v_cndmask_b32_e32 v26, v26, v27, vcc
	v_pk_mul_f32 v[28:29], v[80:81], v[26:27] op_sel_hi:[1,0]
	v_pk_mul_f32 v[70:71], v[70:71], v[26:27] op_sel_hi:[1,0]
	v_pk_mul_f32 v[24:25], v[24:25], v[26:27] op_sel_hi:[1,0]
	v_pk_mul_f32 v[72:73], v[84:85], v[26:27] op_sel_hi:[1,0]
	v_pk_mul_f32 v[22:23], v[22:23], v[26:27] op_sel_hi:[1,0]
	s_waitcnt vmcnt(6)
	v_pk_fma_f32 v[18:19], v[34:35], v[28:29], v[18:19]
	v_pk_fma_f32 v[2:3], v[32:33], v[24:25], v[2:3]
	v_pk_fma_f32 v[24:25], v[30:31], v[70:71], v[62:63]
	v_pk_mul_f32 v[68:69], v[82:83], v[26:27] op_sel_hi:[1,0]
	v_pk_mul_f32 v[74:75], v[86:87], v[26:27] op_sel_hi:[1,0]
	v_pk_mul_f32 v[26:27], v[76:77], v[26:27] op_sel_hi:[1,0]
	s_waitcnt vmcnt(4)
	v_pk_fma_f32 v[28:29], v[42:43], v[72:73], v[64:65]
	v_pk_fma_f32 v[22:23], v[38:39], v[22:23], v[66:67]
	v_mov_b32_e32 v30, v19
	v_mov_b32_e32 v31, v25
	v_pk_fma_f32 v[0:1], v[36:37], v[68:69], v[0:1]
	v_pk_fma_f32 v[6:7], v[40:41], v[26:27], v[6:7]
	v_mov_b32_e32 v26, v18
	v_mov_b32_e32 v27, v24
	v_mov_b32_e32 v38, v23
	v_mov_b32_e32 v39, v29
	v_pk_mul_f32 v[30:31], v[30:31], v[30:31]
	v_pk_fma_f32 v[4:5], v[44:45], v[74:75], v[4:5]
	v_mov_b32_e32 v32, v0
	v_mov_b32_e32 v33, v2
	v_mov_b32_e32 v36, v22
	v_mov_b32_e32 v37, v28
	v_pk_mul_f32 v[38:39], v[38:39], v[38:39]
	v_pk_fma_f32 v[26:27], v[26:27], v[26:27], v[30:31]
	v_mov_b32_e32 v34, v1
	v_mov_b32_e32 v35, v3
	v_mov_b32_e32 v40, v6
	v_mov_b32_e32 v41, v4
	v_pk_fma_f32 v[30:31], v[36:37], v[36:37], v[38:39]
	v_pk_fma_f32 v[26:27], v[32:33], v[32:33], v[26:27]
	v_mov_b32_e32 v42, v7
	v_mov_b32_e32 v43, v5
	v_pk_fma_f32 v[30:31], v[40:41], v[40:41], v[30:31]
	v_pk_fma_f32 v[26:27], v[34:35], v[34:35], v[26:27]
	v_pk_fma_f32 v[30:31], v[42:43], v[42:43], v[30:31]
	v_add_f32_e32 v26, v26, v27
	v_add_f32_e32 v26, v31, v26
	v_add_f32_e32 v26, v30, v26
	s_waitcnt lgkmcnt(0)
	s_nop 1
	v_add_f32_dpp v26, v26, v26 quad_perm:[1,0,3,2] row_mask:0xf bank_mask:0xf
	s_waitcnt lgkmcnt(0)
	s_nop 1
	v_add_f32_dpp v26, v26, v26 quad_perm:[2,3,0,1] row_mask:0xf bank_mask:0xf
	s_waitcnt lgkmcnt(0)
	s_nop 1
	v_add_f32_dpp v26, v26, v26 row_half_mirror row_mask:0xf bank_mask:0xf
	s_waitcnt lgkmcnt(0)
	s_nop 1
	v_add_f32_dpp v26, v26, v26 row_mirror row_mask:0xf bank_mask:0xf
	ds_swizzle_b32 v27, v26 offset:swizzle(SWAP,16)
	s_waitcnt lgkmcnt(0)
	v_add_f32_e32 v26, v26, v27
	ds_bpermute_b32 v27, v89, v26
	s_waitcnt lgkmcnt(0)
	v_add_f32_e32 v26, v26, v27
	v_fmamk_f32 v26, v26, 0x3a800000, v21
	v_mul_f32_e32 v27, 0x4b800000, v26
	v_cmp_gt_f32_e32 vcc, s2, v26
	s_nop 1
	v_cndmask_b32_e32 v26, v26, v27, vcc
	v_rsq_f32_e32 v26, v26
	s_nop 0
	v_mul_f32_e32 v27, 0x45800000, v26
	v_cndmask_b32_e32 v26, v26, v27, vcc
	v_pk_mul_f32 v[18:19], v[18:19], v[26:27] op_sel_hi:[1,0]
	v_pk_mul_f32 v[0:1], v[0:1], v[26:27] op_sel_hi:[1,0]
	v_pk_mul_f32 v[24:25], v[24:25], v[26:27] op_sel_hi:[1,0]
	v_pk_mul_f32 v[30:31], v[2:3], v[26:27] op_sel_hi:[1,0]
	v_pk_mul_f32 v[28:29], v[28:29], v[26:27] op_sel_hi:[1,0]
	v_pk_mul_f32 v[32:33], v[4:5], v[26:27] op_sel_hi:[1,0]
	v_pk_mul_f32 v[34:35], v[22:23], v[26:27] op_sel_hi:[1,0]
	v_pk_mul_f32 v[26:27], v[6:7], v[26:27] op_sel_hi:[1,0]
	s_waitcnt vmcnt(2)
	v_pk_mul_f32 v[2:3], v[52:53], v[0:1]
	v_pk_mul_f32 v[0:1], v[50:51], v[18:19]
	v_pk_mul_f32 v[6:7], v[48:49], v[30:31]
	v_pk_mul_f32 v[4:5], v[46:47], v[24:25]
	s_waitcnt vmcnt(0)
	v_pk_mul_f32 v[24:25], v[60:61], v[32:33]
	v_pk_mul_f32 v[22:23], v[58:59], v[28:29]
	v_pk_mul_f32 v[28:29], v[56:57], v[26:27]
	v_pk_mul_f32 v[26:27], v[54:55], v[34:35]
	global_store_dwordx4 v[16:17], v[0:3], off
	global_store_dwordx4 v[16:17], v[4:7], off offset:16
	global_store_dwordx4 v[16:17], v[22:25], off offset:2048
	global_store_dwordx4 v[16:17], v[26:29], off offset:2064
	v_lshl_add_u64 v[16:17], v[16:17], 0, s[10:11]
	s_andn2_b64 exec, exec, s[0:1]
	s_cbranch_execnz .LBB0_1574
